# speedup vs baseline: 1.1356x; 1.0060x over previous
.LBB5_96:
	s_andn2_b64 vcc, exec, s[4:5]
	s_cbranch_vccnz .LBB5_143
	s_setprio 3
	s_load_dwordx2 s[8:9], s[0:1], 0x0
	s_load_dwordx2 s[10:11], s[0:1], 0x8
	s_load_dwordx2 s[12:13], s[0:1], 0x18
	s_load_dwordx2 s[32:33], s[0:1], 0x28
	s_load_dwordx4 s[36:39], s[0:1], 0x30
	s_load_dwordx2 s[18:19], s[0:1], 0xb8
	s_load_dwordx2 s[16:17], s[0:1], 0xc8
	s_load_dword s34, s[0:1], 0xd4
	s_lshr_b32 s3, s2, 4
	s_bfe_u32 s4, s2, 0x10003
	s_and_b32 s5, s2, 7
	v_lshrrev_b32_e32 v1, 6, v0
	v_and_b32_e32 v2, 63, v0
	v_and_b32_e32 v3, 15, v0
	v_bfe_u32 v4, v0, 4, 2
	s_nop 1
	v_readfirstlane_b32 s6, v1
	s_waitcnt lgkmcnt(0)
	s_cmp_eq_u32 s3, 0
	s_cselect_b32 s12, s12, s32
	s_cselect_b32 s13, s13, s33
	s_cselect_b32 s14, s36, s38
	s_cselect_b32 s15, s37, s39
	s_mul_i32 s35, s4, 0x708
	s_add_u32 s12, s12, s35
	s_addc_u32 s13, s13, 0
	s_mul_i32 s35, s5, 0x25800
	s_add_u32 s14, s14, s35
	s_addc_u32 s15, s15, 0
	s_mul_i32 s35, s4, 0x258
	s_add_u32 s14, s14, s35
	s_addc_u32 s15, s15, 0
	s_lshl_b64 s[10:11], s[10:11], 2
	s_mul_i32 s35, s3, 0x384000
	s_add_u32 s8, s8, s35
	s_addc_u32 s9, s9, 0
	s_mul_i32 s35, s5, 0x70800
	s_add_u32 s8, s8, s35
	s_addc_u32 s9, s9, 0
	s_mul_i32 s35, s4, 0x708
	s_add_u32 s8, s8, s35
	s_addc_u32 s9, s9, 0
	s_mul_i32 s35, s4, 112
	s_lshl_b32 s40, s6, 1
	s_add_i32 s35, s35, s40
	s_mul_i32 s35, s35, 0xe10
	s_add_u32 s22, s8, s35
	s_addc_u32 s23, s9, 0
	s_add_u32 s46, s22, 0xe10
	s_addc_u32 s47, s23, 0
	s_cmp_eq_u32 s4, 0
	s_mov_b32 s27, 0xffff1f00
	s_mov_b32 s20, 0xfffffb50
	s_cselect_b32 s27, 0xe100, s27
	s_cselect_b32 s50, 0, -1
	s_cselect_b32 s20, 0x4b0, s20
	s_cselect_b32 s21, 0, -1
	s_lshl_b32 s35, s3, 1
	s_add_i32 s35, s35, s4
	s_add_i32 s35, s35, s34
	s_mul_i32 s35, s35, 0x28000
	s_add_u32 s16, s16, s35
	s_addc_u32 s17, s17, 0
	s_mul_i32 s35, s6, 0x5000
	s_add_u32 s16, s16, s35
	s_addc_u32 s17, s17, 0
	s_mov_b32 s28, 0xffff
	s_mov_b32 s29, 0
	s_mov_b32 s30, -1
	s_mov_b32 s31, 1
	s_mov_b32 s68, 0x00330033
	s_mov_b32 s69, 0x00330033
	s_mov_b32 s51, 0xbfb8aa3b
	s_mov_b32 s52, 0x4038aa3b
	v_lshlrev_b32_e32 v5, 4, v2
	s_add_u32 s42, s16, 0x0
	s_addc_u32 s43, s17, 0
	global_load_dwordx4 v[16:19], v5, s[42:43] offset:0
	global_load_dwordx4 v[20:23], v5, s[42:43] offset:1024
	global_load_dwordx4 v[24:27], v5, s[42:43] offset:2048
	global_load_dwordx4 v[28:31], v5, s[42:43] offset:3072
	s_add_u32 s42, s16, 0x1000
	s_addc_u32 s43, s17, 0
	global_load_dwordx4 v[80:83], v5, s[42:43]
	s_add_u32 s42, s16, 0x1400
	s_addc_u32 s43, s17, 0
	global_load_dwordx4 v[32:35], v5, s[42:43] offset:0
	global_load_dwordx4 v[36:39], v5, s[42:43] offset:1024
	global_load_dwordx4 v[40:43], v5, s[42:43] offset:2048
	global_load_dwordx4 v[44:47], v5, s[42:43] offset:3072
	s_add_u32 s42, s16, 0x2400
	s_addc_u32 s43, s17, 0
	global_load_dwordx4 v[84:87], v5, s[42:43]
	s_add_u32 s42, s16, 0x2800
	s_addc_u32 s43, s17, 0
	global_load_dwordx4 v[48:51], v5, s[42:43] offset:0
	global_load_dwordx4 v[52:55], v5, s[42:43] offset:1024
	global_load_dwordx4 v[56:59], v5, s[42:43] offset:2048
	global_load_dwordx4 v[60:63], v5, s[42:43] offset:3072
	s_add_u32 s42, s16, 0x3800
	s_addc_u32 s43, s17, 0
	global_load_dwordx4 v[92:95], v5, s[42:43]
	s_add_u32 s42, s16, 0x3c00
	s_addc_u32 s43, s17, 0
	global_load_dwordx4 v[64:67], v5, s[42:43] offset:0
	global_load_dwordx4 v[68:71], v5, s[42:43] offset:1024
	global_load_dwordx4 v[72:75], v5, s[42:43] offset:2048
	global_load_dwordx4 v[76:79], v5, s[42:43] offset:3072
	s_add_u32 s42, s16, 0x4c00
	s_addc_u32 s43, s17, 0
	global_load_dwordx4 v[88:91], v5, s[42:43]
	v_lshlrev_b32_e32 v172, 3, v2
	v_min_u32_e32 v6, 32, v2
	v_lshlrev_b32_e32 v114, 3, v6
	global_load_dwordx2 v[176:177], v172, s[22:23] offset:0
	global_load_dwordx2 v[178:179], v172, s[22:23] offset:512
	global_load_dwordx2 v[180:181], v172, s[22:23] offset:1024
	global_load_dwordx2 v[182:183], v114, s[22:23] offset:1536
	global_load_dwordx2 v[184:185], v172, s[46:47] offset:0
	global_load_dwordx2 v[186:187], v172, s[46:47] offset:512
	global_load_dwordx2 v[188:189], v172, s[46:47] offset:1024
	global_load_dwordx2 v[190:191], v114, s[46:47] offset:1536
	v_and_b32_e32 v6, 1, v3
	v_cmp_eq_u32_e32 vcc, 1, v6
	v_mov_b32_e32 v7, 0x44444444
	v_mov_b32_e32 v8, 0xeeeeeeee
	s_nop 1
	v_cndmask_b32_e32 v112, v7, v8, vcc
	s_mul_i32 s53, s6, 19
	v_add_u32_e32 v6, s53, v3
	v_cmp_gt_u32_e32 vcc, 0x96, v6
	v_add_u32_e32 v7, 0x12c, v6
	v_mov_b32_e32 v8, 0x12c
	s_nop 1
	v_cndmask_b32_e32 v7, v8, v7, vcc
	v_lshlrev_b32_e32 v7, 2, v7
	global_load_dword v9, v7, s[12:13]
	s_mov_b64 s[54:55], vcc
	v_cmp_gt_u32_e32 vcc, 0xc0, v0
	v_lshlrev_b32_e32 v10, 2, v0
	v_mov_b32_e32 v11, 0
	s_and_saveexec_b64 s[44:45], vcc
	ds_write_b32 v10, v11 offset:61440
	s_mov_b64 exec, s[44:45]
	v_and_b32_e32 v10, 31, v0
	v_lshrrev_b32_e32 v11, 5, v0
	v_subrev_u32_e32 v12, 6, v10
	v_max_i32_e32 v12, 0, v12
	v_mul_u32_u24_e32 v13, 11, v12
	v_lshrrev_b32_e32 v13, 5, v13
	v_mul_u32_u24_e32 v14, 3, v13
	v_sub_u32_e32 v14, v12, v14
	v_mul_u32_u24_e32 v15, 19, v13
	v_add3_u32 v15, v15, v14, 16
	v_cmp_gt_u32_e32 vcc, 0x96, v15
	v_cmp_lt_u32_e64 s[56:57], 5, v10
	v_cmp_gt_u32_e64 s[58:59], 30, v10
	s_and_b64 s[56:57], s[56:57], vcc
	s_and_b64 s[56:57], s[56:57], s[58:59]
	v_add_u32_e32 v15, 0x12c, v15
	v_mov_b32_e32 v14, 0x12c
	v_cndmask_b32_e64 v15, v14, v15, s[56:57]
	v_lshlrev_b32_e32 v15, 2, v15
	global_load_dword v14, v15, s[12:13]
	v_mul_u32_u24_e32 v11, 0x780, v11
	v_lshl_add_u32 v11, v10, 2, v11
	s_waitcnt vmcnt(0)
	v_mul_f32_e32 v14, s52, v14
	v_mul_f32_e32 v9, s52, v9
	v_cndmask_b32_e64 v14, 0, v14, s[56:57]
	v_cndmask_b32_e64 v113, 0, v9, s[54:55]
	s_and_saveexec_b64 s[44:45], s[58:59]
	ds_write_b32 v11, v14 offset:1800
	ds_write_b32 v11, v14 offset:32520
	s_mov_b64 exec, s[44:45]
	v_lshlrev_b32_e32 v172, 3, v2
	s_lshl_b32 s35, s6, 1
	s_sub_i32 s40, 15, s35
	s_cmp_eq_u32 s4, 0
	s_cselect_b32 s41, s35, s40
	s_add_i32 s35, s35, 1
	s_sub_i32 s40, 15, s35
	s_cmp_eq_u32 s4, 0
	s_cselect_b32 s40, s35, s40
	s_mul_i32 s41, s41, 0x780
	s_mul_i32 s40, s40, 0x780
	v_add_u32_e32 v173, s41, v172
	v_add_u32_e32 v174, s40, v172
	v_min_u32_e32 v6, 32, v2
	v_lshlrev_b32_e32 v114, 3, v6
	v_add_u32_e32 v115, s41, v114
	v_add_u32_e32 v169, s40, v114
	v_cmp_lt_u32_e32 vcc, 21, v2
	v_mov_b32_e32 v6, s51
	v_mov_b32_e32 v7, s52
	s_nop 0
	v_cndmask_b32_e32 v175, v6, v7, vcc
	s_waitcnt vmcnt(0)
	v_mul_f32_e32 v176, s51, v176
	v_mul_f32_e32 v177, s51, v177
	v_mul_f32_e32 v178, s51, v178
	v_mul_f32_e32 v179, s51, v179
	v_mul_f32_e32 v180, v175, v180
	v_mul_f32_e32 v181, v175, v181
	v_mul_f32_e32 v182, s52, v182
	v_mul_f32_e32 v183, s52, v183
	ds_write_b64 v173, v[176:177] offset:0
	ds_write_b64 v173, v[178:179] offset:512
	ds_write_b64 v173, v[180:181] offset:1024
	ds_write_b64 v115, v[182:183] offset:1536
	v_mul_f32_e32 v184, s51, v184
	v_mul_f32_e32 v185, s51, v185
	v_mul_f32_e32 v186, s51, v186
	v_mul_f32_e32 v187, s51, v187
	v_mul_f32_e32 v188, v175, v188
	v_mul_f32_e32 v189, v175, v189
	v_mul_f32_e32 v190, s52, v190
	v_mul_f32_e32 v191, s52, v191
	ds_write_b64 v174, v[184:185] offset:0
	ds_write_b64 v174, v[186:187] offset:512
	ds_write_b64 v174, v[188:189] offset:1024
	ds_write_b64 v169, v[190:191] offset:1536
	s_movk_i32 s55, 0x7800
	v_add_u32_e32 v173, s55, v173
	v_add_u32_e32 v174, s55, v174
	v_add_u32_e32 v115, s55, v115
	v_add_u32_e32 v169, s55, v169
	s_sub_i32 s55, 0, s55
	v_add_u32_e32 v6, s53, v2
	v_cmp_gt_u32_e32 vcc, 0x96, v6
	v_cmp_gt_u32_e64 s[56:57], 16, v2
	v_cmp_gt_u32_e64 s[58:59], 19, v2
	s_and_b64 s[56:57], s[56:57], vcc
	s_and_b64 s[58:59], s[58:59], vcc
	v_mov_b32_e32 v7, 0x710
	v_lshlrev_b32_e32 v8, 2, v6
	v_add_u32_e32 v9, 0x258, v8
	v_add_u32_e32 v10, 0x4b0, v8
	v_cndmask_b32_e64 v163, v7, v8, s[56:57]
	v_cndmask_b32_e64 v164, v7, v9, s[56:57]
	v_cndmask_b32_e64 v166, v7, v10, s[58:59]
	v_subrev_u32_e32 v9, 16, v2
	v_cmp_gt_u32_e64 s[60:61], 6, v9
	v_cmp_lt_u32_e32 vcc, 2, v9
	v_mov_b32_e32 v11, 0x93
	s_nop 0
	v_cndmask_b32_e32 v10, 0, v11, vcc
	v_cndmask_b32_e64 v12, 0, 3, vcc
	v_sub_u32_e32 v13, v6, v12
	v_cmp_gt_u32_e32 vcc, 0x96, v13
	s_and_b64 s[60:61], s[60:61], vcc
	v_add_u32_e32 v13, v6, v10
	v_lshlrev_b32_e32 v13, 2, v13
	v_cndmask_b32_e64 v165, v7, v13, s[60:61]
	v_subrev_u32_e32 v9, 22, v2
	v_cmp_gt_u32_e32 vcc, 3, v9
	s_mul_i32 s35, s6, 3
	s_addk_i32 s35, 0x1c8
	v_add_lshl_u32 v9, v9, s35, 2
	s_nop 0
	v_cndmask_b32_e32 v165, v165, v9, vcc
	v_and_b32_e32 v9, 1, v3
	v_lshlrev_b32_e32 v9, 4, v9
	v_lshl_or_b32 v9, v4, 5, v9
	v_add_u32_e32 v167, 0xf000, v9
	v_and_b32_e32 v9, 0xfffffff0, v6
	v_bfe_u32 v10, v6, 1, 1
	v_lshl_or_b32 v9, v10, 3, v9
	v_bfe_u32 v10, v6, 2, 2
	v_lshl_or_b32 v9, v10, 1, v9
	v_and_b32_e32 v10, 1, v6
	v_or_b32_e32 v9, v9, v10
	v_lshlrev_b32_e32 v9, 1, v9
	v_add_u32_e32 v9, 0xf000, v9
	v_lshlrev_b32_e32 v10, 1, v2
	v_add_u32_e32 v10, 0xf300, v10
	v_cndmask_b32_e64 v168, v10, v9, s[58:59]
	v_cmp_gt_u32_e32 vcc, 136, v0
	v_lshlrev_b32_e32 v9, 2, v0
	v_mov_b32_e32 v10, 0
	s_and_saveexec_b64 s[44:45], vcc
	ds_write_b32 v9, v10 offset:62720
	s_mov_b64 exec, s[44:45]
	v_and_b32_e32 v9, 14, v3
	v_cmp_eq_u32_e64 s[62:63], 2, v9
	v_mov_b32_e32 v10, 0xf500
	s_nop 1
	v_cndmask_b32_e64 v167, v167, v10, s[62:63]
	v_cmp_eq_u32_e64 s[64:65], 0, v9
	v_cmp_eq_u32_e64 s[66:67], 4, v9
	s_or_b64 s[64:65], s[64:65], s[66:67]
	v_cmp_gt_u32_e64 s[66:67], 2, v4
	s_and_b64 s[64:65], s[64:65], s[66:67]
	s_andn2_b64 s[66:67], s[62:63], s[66:67]
	s_or_b64 s[64:65], s[64:65], s[66:67]
	v_and_b32_e32 v9, 1, v4
	v_lshlrev_b32_e32 v9, 5, v9
	v_and_b32_e32 v11, 1, v3
	v_lshl_or_b32 v9, v11, 4, v9
	v_add_u32_e32 v9, 0xf100, v9
	v_cndmask_b32_e64 v96, v10, v9, s[64:65]
	s_mul_i32 s35, s4, 0x25350
	s_add_u32 s14, s14, s35
	s_addc_u32 s15, s15, 0
	s_add_u32 s18, s18, 0x25800
	s_addc_u32 s19, s19, 0
	v_lshlrev_b32_e32 v9, 2, v0
	v_mov_b32_e32 v10, s18
	v_mov_b32_e32 v11, s19
	v_mov_b32_e32 v12, s14
	v_mov_b32_e32 v13, s15
	v_cndmask_b32_e64 v9, v9, v8, s[58:59]
	v_cndmask_b32_e64 v10, v10, v12, s[58:59]
	v_cndmask_b32_e64 v11, v11, v13, s[58:59]
	v_add_co_u32_e32 v170, vcc, v10, v9
	s_nop 1
	v_addc_co_u32_e32 v171, vcc, 0, v11, vcc
	v_mov_b32_e32 v161, 0
	v_mov_b32_e32 v137, 0
	v_mov_b32_e32 v138, 0
	v_mov_b32_e32 v139, 0
	v_mov_b32_e32 v141, 0
	v_mov_b32_e32 v142, 0
	v_mov_b32_e32 v143, 0
	v_mov_b32_e32 v145, 0
	v_mov_b32_e32 v146, 0
	v_mov_b32_e32 v147, 0
	v_mov_b32_e32 v149, 0
	v_mov_b32_e32 v150, 0
	v_mov_b32_e32 v151, 0
	v_mov_b32_e32 v209, 0
	v_mov_b32_e32 v210, 0
	v_mov_b32_e32 v211, 0
	v_mov_b32_e32 v213, 0
	v_mov_b32_e32 v214, 0
	v_mov_b32_e32 v215, 0
	v_mov_b32_e32 v217, 0
	v_mov_b32_e32 v218, 0
	v_mov_b32_e32 v219, 0
	v_mov_b32_e32 v221, 0
	v_mov_b32_e32 v222, 0
	v_mov_b32_e32 v223, 0
	s_mov_b32 s26, 0
	s_waitcnt vmcnt(0) lgkmcnt(0)
	s_barrier
	ds_read_b32 v136, v163 offset:0
	ds_read_b32 v140, v164 offset:0
	ds_read_b32 v148, v165 offset:0
	ds_read_b32 v152, v166 offset:0
	v_mov_b32_e32 v144, v113
	s_waitcnt lgkmcnt(0)
.Lgru1_chunk:
	ds_read_b128 v[116:119], v167 offset:0
	ds_read_b128 v[120:123], v167 offset:128
	ds_read_b128 v[124:127], v96 offset:0
	s_waitcnt lgkmcnt(2)
	v_smfmac_f32_16x16x64_f16 v[136:139], v[116:119], v[16:23], v112
	v_smfmac_f32_16x16x64_f16 v[148:151], v[116:119], v[64:71], v112
	s_waitcnt lgkmcnt(1)
	v_smfmac_f32_16x16x64_f16 v[136:139], v[120:123], v[24:31], v112
	v_smfmac_f32_16x16x64_f16 v[148:151], v[120:123], v[72:79], v112
	s_waitcnt lgkmcnt(0)
	v_smfmac_f32_16x16x64_f16 v[136:139], v[124:127], v[80:87], v112
	ds_read_b32 v208, v163 offset:1920
	v_smfmac_f32_16x16x64_f16 v[148:151], v[124:127], v[88:95], v112
	ds_read_b32 v220, v165 offset:1920
	v_smfmac_f32_16x16x64_f16 v[144:147], v[116:119], v[48:55], v112
	ds_read_b32 v212, v164 offset:1920
	ds_read_b32 v224, v166 offset:1920
	v_mov_b32_e32 v216, v113
	v_smfmac_f32_16x16x64_f16 v[140:143], v[116:119], v[32:39], v112
	v_mov_b32_e32 v209, 0
	v_mov_b32_e32 v213, 0
	v_mov_b32_e32 v217, 0
	v_mov_b32_e32 v221, 0
	s_cmp_eq_u32 s26, 0
	s_cbranch_scc1 .Lgru1_nostore
	global_store_dword v[170:171], v161, off
	v_lshl_add_u64 v[170:171], v[170:171], 0, s[20:21]
.Lgru1_nostore:
	v_add_f32_e32 v156, v148, v149
	v_add_f32_e32 v159, v136, v137
	v_smfmac_f32_16x16x64_f16 v[144:147], v[120:123], v[56:63], v112
	v_add_f32_e32 v97, v138, v139
	v_add_f32_e32 v98, v150, v151
	v_mov_b32_dpp v159, v156 quad_perm:[0,1,2,3] row_mask:0x2 bank_mask:0xf
	v_exp_f32_e32 v159, v159
	v_smfmac_f32_16x16x64_f16 v[140:143], v[120:123], v[40:47], v112
	v_mov_b32_e32 v210, 0
	v_mov_b32_e32 v211, 0
	v_mov_b32_e32 v222, 0
	v_mov_b32_e32 v223, 0
	v_add_f32_e32 v159, 1.0, v159
	v_rcp_f32_e32 v159, v159
	s_nop 0
	v_add_f32_e32 v155, v144, v145
	v_add_f32_e32 v155, v155, v98
	v_mov_b32_dpp v155, v156 row_shl:6 row_mask:0x2 bank_mask:0xf
	v_fmac_f32_e32 v152, v159, v155
	v_exp_f32_e32 v152, v152
	v_add_f32_e32 v160, v140, v141
	v_add_f32_e32 v160, v160, v97
	v_mov_b32_dpp v160, v156 row_shl:3 row_mask:0x2 bank_mask:0xf
	v_add_f32_e32 v152, 1.0, v152
	v_rcp_f32_e32 v159, v152
	v_exp_f32_e32 v160, v160
	v_fma_f32 v159, v159, -2.0, 1.0
	v_add_f32_e32 v160, 1.0, v160
	v_rcp_f32_e32 v160, v160
	v_sub_f32_e32 v153, v161, v159
	v_fma_f32 v161, v160, v153, v159
	v_fma_mixlo_f16 v162, v160, v153, v159
	ds_write_b16 v168, v162 offset:384
	s_waitcnt lgkmcnt(0)
	s_barrier
	ds_read_b128 v[116:119], v167 offset:384
	ds_read_b128 v[120:123], v167 offset:512
	ds_read_b128 v[124:127], v96 offset:384
	s_waitcnt lgkmcnt(2)
	v_smfmac_f32_16x16x64_f16 v[208:211], v[116:119], v[16:23], v112
	v_smfmac_f32_16x16x64_f16 v[220:223], v[116:119], v[64:71], v112
	s_waitcnt lgkmcnt(1)
	v_smfmac_f32_16x16x64_f16 v[208:211], v[120:123], v[24:31], v112
	v_smfmac_f32_16x16x64_f16 v[220:223], v[120:123], v[72:79], v112
	s_waitcnt lgkmcnt(0)
	v_smfmac_f32_16x16x64_f16 v[208:211], v[124:127], v[80:87], v112
	ds_read_b32 v136, v163 offset:3840
	v_smfmac_f32_16x16x64_f16 v[220:223], v[124:127], v[88:95], v112
	ds_read_b32 v148, v165 offset:3840
	s_cmp_eq_u32 s26, 7
	s_cbranch_scc1 .Lgru1_nopf
	s_add_u32 s22, s22, s27
	s_addc_u32 s23, s23, s50
	s_add_u32 s46, s46, s27
	s_addc_u32 s47, s47, s50
	global_load_dwordx2 v[176:177], v172, s[22:23] offset:0
	global_load_dwordx2 v[178:179], v172, s[22:23] offset:512
	global_load_dwordx2 v[180:181], v172, s[22:23] offset:1024
	global_load_dwordx2 v[184:185], v172, s[46:47] offset:0
	global_load_dwordx2 v[186:187], v172, s[46:47] offset:512
	global_load_dwordx2 v[188:189], v172, s[46:47] offset:1024
	global_load_dwordx2 v[182:183], v114, s[22:23] offset:1536
	global_load_dwordx2 v[190:191], v114, s[46:47] offset:1536
.Lgru1_nopf:
	v_smfmac_f32_16x16x64_f16 v[216:219], v[116:119], v[48:55], v112
	ds_read_b32 v140, v164 offset:3840
	ds_read_b32 v152, v166 offset:3840
	v_mov_b32_e32 v144, v113
	v_smfmac_f32_16x16x64_f16 v[212:215], v[116:119], v[32:39], v112
	v_mov_b32_e32 v137, 0
	v_mov_b32_e32 v141, 0
	v_mov_b32_e32 v145, 0
	v_mov_b32_e32 v149, 0
	global_store_dword v[170:171], v161, off
	v_lshl_add_u64 v[170:171], v[170:171], 0, s[20:21]
	v_add_f32_e32 v156, v220, v221
	v_add_f32_e32 v159, v208, v209
	v_smfmac_f32_16x16x64_f16 v[216:219], v[120:123], v[56:63], v112
	v_add_f32_e32 v97, v210, v211
	v_add_f32_e32 v98, v222, v223
	v_mov_b32_dpp v159, v156 quad_perm:[0,1,2,3] row_mask:0x2 bank_mask:0xf
	v_exp_f32_e32 v159, v159
	v_smfmac_f32_16x16x64_f16 v[212:215], v[120:123], v[40:47], v112
	v_mov_b32_e32 v138, 0
	v_mov_b32_e32 v139, 0
	v_mov_b32_e32 v150, 0
	v_mov_b32_e32 v151, 0
	v_add_f32_e32 v159, 1.0, v159
	v_rcp_f32_e32 v159, v159
	s_nop 0
	v_add_f32_e32 v155, v216, v217
	v_add_f32_e32 v155, v155, v98
	v_mov_b32_dpp v155, v156 row_shl:6 row_mask:0x2 bank_mask:0xf
	v_fmac_f32_e32 v224, v159, v155
	v_exp_f32_e32 v224, v224
	v_add_f32_e32 v160, v212, v213
	v_add_f32_e32 v160, v160, v97
	v_mov_b32_dpp v160, v156 row_shl:3 row_mask:0x2 bank_mask:0xf
	v_add_f32_e32 v224, 1.0, v224
	v_rcp_f32_e32 v159, v224
	v_exp_f32_e32 v160, v160
	v_fma_f32 v159, v159, -2.0, 1.0
	v_add_f32_e32 v160, 1.0, v160
	v_rcp_f32_e32 v160, v160
	v_sub_f32_e32 v153, v161, v159
	v_fma_f32 v161, v160, v153, v159
	v_fma_mixlo_f16 v162, v160, v153, v159
	ds_write_b16 v168, v162 offset:0
	s_waitcnt lgkmcnt(0)
	s_barrier
	ds_read_b128 v[116:119], v167 offset:0
	ds_read_b128 v[120:123], v167 offset:128
	ds_read_b128 v[124:127], v96 offset:0
	s_waitcnt lgkmcnt(2)
	v_smfmac_f32_16x16x64_f16 v[136:139], v[116:119], v[16:23], v112
	v_smfmac_f32_16x16x64_f16 v[148:151], v[116:119], v[64:71], v112
	s_waitcnt lgkmcnt(1)
	v_smfmac_f32_16x16x64_f16 v[136:139], v[120:123], v[24:31], v112
	v_smfmac_f32_16x16x64_f16 v[148:151], v[120:123], v[72:79], v112
	s_waitcnt lgkmcnt(0)
	v_smfmac_f32_16x16x64_f16 v[136:139], v[124:127], v[80:87], v112
	ds_read_b32 v208, v163 offset:5760
	v_smfmac_f32_16x16x64_f16 v[148:151], v[124:127], v[88:95], v112
	ds_read_b32 v220, v165 offset:5760
	v_smfmac_f32_16x16x64_f16 v[144:147], v[116:119], v[48:55], v112
	ds_read_b32 v212, v164 offset:5760
	ds_read_b32 v224, v166 offset:5760
	v_mov_b32_e32 v216, v113
	v_smfmac_f32_16x16x64_f16 v[140:143], v[116:119], v[32:39], v112
	v_mov_b32_e32 v209, 0
	v_mov_b32_e32 v213, 0
	v_mov_b32_e32 v217, 0
	v_mov_b32_e32 v221, 0
	global_store_dword v[170:171], v161, off
	v_lshl_add_u64 v[170:171], v[170:171], 0, s[20:21]
	v_add_f32_e32 v156, v148, v149
	v_add_f32_e32 v159, v136, v137
	v_smfmac_f32_16x16x64_f16 v[144:147], v[120:123], v[56:63], v112
	v_add_f32_e32 v97, v138, v139
	v_add_f32_e32 v98, v150, v151
	v_mov_b32_dpp v159, v156 quad_perm:[0,1,2,3] row_mask:0x2 bank_mask:0xf
	v_exp_f32_e32 v159, v159
	v_smfmac_f32_16x16x64_f16 v[140:143], v[120:123], v[40:47], v112
	v_mov_b32_e32 v210, 0
	v_mov_b32_e32 v211, 0
	v_mov_b32_e32 v222, 0
	v_mov_b32_e32 v223, 0
	v_add_f32_e32 v159, 1.0, v159
	v_rcp_f32_e32 v159, v159
	s_nop 0
	v_add_f32_e32 v155, v144, v145
	v_add_f32_e32 v155, v155, v98
	v_mov_b32_dpp v155, v156 row_shl:6 row_mask:0x2 bank_mask:0xf
	v_fmac_f32_e32 v152, v159, v155
	v_exp_f32_e32 v152, v152
	v_add_f32_e32 v160, v140, v141
	v_add_f32_e32 v160, v160, v97
	v_mov_b32_dpp v160, v156 row_shl:3 row_mask:0x2 bank_mask:0xf
	v_add_f32_e32 v152, 1.0, v152
	v_rcp_f32_e32 v159, v152
	v_exp_f32_e32 v160, v160
	v_fma_f32 v159, v159, -2.0, 1.0
	v_add_f32_e32 v160, 1.0, v160
	v_rcp_f32_e32 v160, v160
	v_sub_f32_e32 v153, v161, v159
	v_fma_f32 v161, v160, v153, v159
	v_fma_mixlo_f16 v162, v160, v153, v159
	ds_write_b16 v168, v162 offset:384
	s_waitcnt lgkmcnt(0)
	s_barrier
	ds_read_b128 v[116:119], v167 offset:384
	ds_read_b128 v[120:123], v167 offset:512
	ds_read_b128 v[124:127], v96 offset:384
	s_waitcnt lgkmcnt(2)
	v_smfmac_f32_16x16x64_f16 v[208:211], v[116:119], v[16:23], v112
	v_smfmac_f32_16x16x64_f16 v[220:223], v[116:119], v[64:71], v112
	s_waitcnt lgkmcnt(1)
	v_smfmac_f32_16x16x64_f16 v[208:211], v[120:123], v[24:31], v112
	v_smfmac_f32_16x16x64_f16 v[220:223], v[120:123], v[72:79], v112
	s_waitcnt lgkmcnt(0)
	v_smfmac_f32_16x16x64_f16 v[208:211], v[124:127], v[80:87], v112
	ds_read_b32 v136, v163 offset:7680
	v_smfmac_f32_16x16x64_f16 v[220:223], v[124:127], v[88:95], v112
	ds_read_b32 v148, v165 offset:7680
	v_smfmac_f32_16x16x64_f16 v[216:219], v[116:119], v[48:55], v112
	ds_read_b32 v140, v164 offset:7680
	ds_read_b32 v152, v166 offset:7680
	v_mov_b32_e32 v144, v113
	v_smfmac_f32_16x16x64_f16 v[212:215], v[116:119], v[32:39], v112
	v_mov_b32_e32 v137, 0
	v_mov_b32_e32 v141, 0
	v_mov_b32_e32 v145, 0
	v_mov_b32_e32 v149, 0
	global_store_dword v[170:171], v161, off
	v_lshl_add_u64 v[170:171], v[170:171], 0, s[20:21]
	v_add_f32_e32 v156, v220, v221
	v_add_f32_e32 v159, v208, v209
	v_smfmac_f32_16x16x64_f16 v[216:219], v[120:123], v[56:63], v112
	v_add_f32_e32 v97, v210, v211
	v_add_f32_e32 v98, v222, v223
	v_mov_b32_dpp v159, v156 quad_perm:[0,1,2,3] row_mask:0x2 bank_mask:0xf
	v_exp_f32_e32 v159, v159
	v_smfmac_f32_16x16x64_f16 v[212:215], v[120:123], v[40:47], v112
	v_mov_b32_e32 v138, 0
	v_mov_b32_e32 v139, 0
	v_mov_b32_e32 v150, 0
	v_mov_b32_e32 v151, 0
	v_add_f32_e32 v159, 1.0, v159
	v_rcp_f32_e32 v159, v159
	s_nop 0
	v_add_f32_e32 v155, v216, v217
	v_add_f32_e32 v155, v155, v98
	v_mov_b32_dpp v155, v156 row_shl:6 row_mask:0x2 bank_mask:0xf
	v_fmac_f32_e32 v224, v159, v155
	v_exp_f32_e32 v224, v224
	v_add_f32_e32 v160, v212, v213
	v_add_f32_e32 v160, v160, v97
	v_mov_b32_dpp v160, v156 row_shl:3 row_mask:0x2 bank_mask:0xf
	v_add_f32_e32 v224, 1.0, v224
	v_rcp_f32_e32 v159, v224
	v_exp_f32_e32 v160, v160
	v_fma_f32 v159, v159, -2.0, 1.0
	v_add_f32_e32 v160, 1.0, v160
	v_rcp_f32_e32 v160, v160
	v_sub_f32_e32 v153, v161, v159
	v_fma_f32 v161, v160, v153, v159
	v_fma_mixlo_f16 v162, v160, v153, v159
	ds_write_b16 v168, v162 offset:0
	s_waitcnt lgkmcnt(0)
	s_barrier
	ds_read_b128 v[116:119], v167 offset:0
	ds_read_b128 v[120:123], v167 offset:128
	ds_read_b128 v[124:127], v96 offset:0
	s_waitcnt lgkmcnt(2)
	v_smfmac_f32_16x16x64_f16 v[136:139], v[116:119], v[16:23], v112
	v_smfmac_f32_16x16x64_f16 v[148:151], v[116:119], v[64:71], v112
	s_waitcnt lgkmcnt(1)
	v_smfmac_f32_16x16x64_f16 v[136:139], v[120:123], v[24:31], v112
	v_smfmac_f32_16x16x64_f16 v[148:151], v[120:123], v[72:79], v112
	s_waitcnt lgkmcnt(0)
	v_smfmac_f32_16x16x64_f16 v[136:139], v[124:127], v[80:87], v112
	ds_read_b32 v208, v163 offset:9600
	v_smfmac_f32_16x16x64_f16 v[148:151], v[124:127], v[88:95], v112
	ds_read_b32 v220, v165 offset:9600
	v_smfmac_f32_16x16x64_f16 v[144:147], v[116:119], v[48:55], v112
	ds_read_b32 v212, v164 offset:9600
	ds_read_b32 v224, v166 offset:9600
	v_mov_b32_e32 v216, v113
	v_smfmac_f32_16x16x64_f16 v[140:143], v[116:119], v[32:39], v112
	v_mov_b32_e32 v209, 0
	v_mov_b32_e32 v213, 0
	v_mov_b32_e32 v217, 0
	v_mov_b32_e32 v221, 0
	global_store_dword v[170:171], v161, off
	v_lshl_add_u64 v[170:171], v[170:171], 0, s[20:21]
	v_add_f32_e32 v156, v148, v149
	v_add_f32_e32 v159, v136, v137
	v_smfmac_f32_16x16x64_f16 v[144:147], v[120:123], v[56:63], v112
	v_add_f32_e32 v97, v138, v139
	v_add_f32_e32 v98, v150, v151
	v_mov_b32_dpp v159, v156 quad_perm:[0,1,2,3] row_mask:0x2 bank_mask:0xf
	v_exp_f32_e32 v159, v159
	v_smfmac_f32_16x16x64_f16 v[140:143], v[120:123], v[40:47], v112
	v_mov_b32_e32 v210, 0
	v_mov_b32_e32 v211, 0
	v_mov_b32_e32 v222, 0
	v_mov_b32_e32 v223, 0
	v_add_f32_e32 v159, 1.0, v159
	v_rcp_f32_e32 v159, v159
	s_nop 0
	v_add_f32_e32 v155, v144, v145
	v_add_f32_e32 v155, v155, v98
	v_mov_b32_dpp v155, v156 row_shl:6 row_mask:0x2 bank_mask:0xf
	v_fmac_f32_e32 v152, v159, v155
	v_exp_f32_e32 v152, v152
	v_add_f32_e32 v160, v140, v141
	v_add_f32_e32 v160, v160, v97
	v_mov_b32_dpp v160, v156 row_shl:3 row_mask:0x2 bank_mask:0xf
	v_add_f32_e32 v152, 1.0, v152
	v_rcp_f32_e32 v159, v152
	v_exp_f32_e32 v160, v160
	v_fma_f32 v159, v159, -2.0, 1.0
	v_add_f32_e32 v160, 1.0, v160
	v_rcp_f32_e32 v160, v160
	v_sub_f32_e32 v153, v161, v159
	v_fma_f32 v161, v160, v153, v159
	v_fma_mixlo_f16 v162, v160, v153, v159
	ds_write_b16 v168, v162 offset:384
	s_waitcnt lgkmcnt(0)
	s_barrier
	ds_read_b128 v[116:119], v167 offset:384
	ds_read_b128 v[120:123], v167 offset:512
	ds_read_b128 v[124:127], v96 offset:384
	s_waitcnt lgkmcnt(2)
	v_smfmac_f32_16x16x64_f16 v[208:211], v[116:119], v[16:23], v112
	v_smfmac_f32_16x16x64_f16 v[220:223], v[116:119], v[64:71], v112
	s_waitcnt lgkmcnt(1)
	v_smfmac_f32_16x16x64_f16 v[208:211], v[120:123], v[24:31], v112
	v_smfmac_f32_16x16x64_f16 v[220:223], v[120:123], v[72:79], v112
	s_waitcnt lgkmcnt(0)
	v_smfmac_f32_16x16x64_f16 v[208:211], v[124:127], v[80:87], v112
	ds_read_b32 v136, v163 offset:11520
	v_smfmac_f32_16x16x64_f16 v[220:223], v[124:127], v[88:95], v112
	ds_read_b32 v148, v165 offset:11520
	v_smfmac_f32_16x16x64_f16 v[216:219], v[116:119], v[48:55], v112
	ds_read_b32 v140, v164 offset:11520
	ds_read_b32 v152, v166 offset:11520
	v_mov_b32_e32 v144, v113
	v_smfmac_f32_16x16x64_f16 v[212:215], v[116:119], v[32:39], v112
	v_mov_b32_e32 v137, 0
	v_mov_b32_e32 v141, 0
	v_mov_b32_e32 v145, 0
	v_mov_b32_e32 v149, 0
	global_store_dword v[170:171], v161, off
	v_lshl_add_u64 v[170:171], v[170:171], 0, s[20:21]
	v_add_f32_e32 v156, v220, v221
	v_add_f32_e32 v159, v208, v209
	v_smfmac_f32_16x16x64_f16 v[216:219], v[120:123], v[56:63], v112
	v_add_f32_e32 v97, v210, v211
	v_add_f32_e32 v98, v222, v223
	v_mov_b32_dpp v159, v156 quad_perm:[0,1,2,3] row_mask:0x2 bank_mask:0xf
	v_exp_f32_e32 v159, v159
	v_smfmac_f32_16x16x64_f16 v[212:215], v[120:123], v[40:47], v112
	v_mov_b32_e32 v138, 0
	v_mov_b32_e32 v139, 0
	v_mov_b32_e32 v150, 0
	v_mov_b32_e32 v151, 0
	v_add_f32_e32 v159, 1.0, v159
	v_rcp_f32_e32 v159, v159
	s_nop 0
	v_add_f32_e32 v155, v216, v217
	v_add_f32_e32 v155, v155, v98
	v_mov_b32_dpp v155, v156 row_shl:6 row_mask:0x2 bank_mask:0xf
	v_fmac_f32_e32 v224, v159, v155
	v_exp_f32_e32 v224, v224
	v_add_f32_e32 v160, v212, v213
	v_add_f32_e32 v160, v160, v97
	v_mov_b32_dpp v160, v156 row_shl:3 row_mask:0x2 bank_mask:0xf
	v_add_f32_e32 v224, 1.0, v224
	v_rcp_f32_e32 v159, v224
	v_exp_f32_e32 v160, v160
	v_fma_f32 v159, v159, -2.0, 1.0
	v_add_f32_e32 v160, 1.0, v160
	v_rcp_f32_e32 v160, v160
	v_sub_f32_e32 v153, v161, v159
	v_fma_f32 v161, v160, v153, v159
	v_fma_mixlo_f16 v162, v160, v153, v159
	ds_write_b16 v168, v162 offset:0
	s_waitcnt lgkmcnt(0)
	s_barrier
	ds_read_b128 v[116:119], v167 offset:0
	ds_read_b128 v[120:123], v167 offset:128
	ds_read_b128 v[124:127], v96 offset:0
	s_waitcnt lgkmcnt(2)
	v_smfmac_f32_16x16x64_f16 v[136:139], v[116:119], v[16:23], v112
	v_smfmac_f32_16x16x64_f16 v[148:151], v[116:119], v[64:71], v112
	s_waitcnt lgkmcnt(1)
	v_smfmac_f32_16x16x64_f16 v[136:139], v[120:123], v[24:31], v112
	v_smfmac_f32_16x16x64_f16 v[148:151], v[120:123], v[72:79], v112
	s_waitcnt lgkmcnt(0)
	v_smfmac_f32_16x16x64_f16 v[136:139], v[124:127], v[80:87], v112
	ds_read_b32 v208, v163 offset:13440
	v_smfmac_f32_16x16x64_f16 v[148:151], v[124:127], v[88:95], v112
	ds_read_b32 v220, v165 offset:13440
	v_smfmac_f32_16x16x64_f16 v[144:147], v[116:119], v[48:55], v112
	ds_read_b32 v212, v164 offset:13440
	ds_read_b32 v224, v166 offset:13440
	v_mov_b32_e32 v216, v113
	v_smfmac_f32_16x16x64_f16 v[140:143], v[116:119], v[32:39], v112
	v_mov_b32_e32 v209, 0
	v_mov_b32_e32 v213, 0
	v_mov_b32_e32 v217, 0
	v_mov_b32_e32 v221, 0
	global_store_dword v[170:171], v161, off
	v_lshl_add_u64 v[170:171], v[170:171], 0, s[20:21]
	v_add_f32_e32 v156, v148, v149
	v_add_f32_e32 v159, v136, v137
	v_smfmac_f32_16x16x64_f16 v[144:147], v[120:123], v[56:63], v112
	v_add_f32_e32 v97, v138, v139
	v_add_f32_e32 v98, v150, v151
	v_mov_b32_dpp v159, v156 quad_perm:[0,1,2,3] row_mask:0x2 bank_mask:0xf
	v_exp_f32_e32 v159, v159
	v_smfmac_f32_16x16x64_f16 v[140:143], v[120:123], v[40:47], v112
	v_mov_b32_e32 v210, 0
	v_mov_b32_e32 v211, 0
	v_mov_b32_e32 v222, 0
	v_mov_b32_e32 v223, 0
	v_add_f32_e32 v159, 1.0, v159
	v_rcp_f32_e32 v159, v159
	s_nop 0
	v_add_f32_e32 v155, v144, v145
	v_add_f32_e32 v155, v155, v98
	v_mov_b32_dpp v155, v156 row_shl:6 row_mask:0x2 bank_mask:0xf
	v_fmac_f32_e32 v152, v159, v155
	v_exp_f32_e32 v152, v152
	v_add_f32_e32 v160, v140, v141
	v_add_f32_e32 v160, v160, v97
	v_mov_b32_dpp v160, v156 row_shl:3 row_mask:0x2 bank_mask:0xf
	v_add_f32_e32 v152, 1.0, v152
	v_rcp_f32_e32 v159, v152
	v_exp_f32_e32 v160, v160
	v_fma_f32 v159, v159, -2.0, 1.0
	v_add_f32_e32 v160, 1.0, v160
	v_rcp_f32_e32 v160, v160
	v_sub_f32_e32 v153, v161, v159
	v_fma_f32 v161, v160, v153, v159
	v_fma_mixlo_f16 v162, v160, v153, v159
	ds_write_b16 v168, v162 offset:384
	s_waitcnt lgkmcnt(0)
	s_barrier
	ds_read_b128 v[116:119], v167 offset:384
	ds_read_b128 v[120:123], v167 offset:512
	ds_read_b128 v[124:127], v96 offset:384
	s_waitcnt lgkmcnt(2)
	v_smfmac_f32_16x16x64_f16 v[208:211], v[116:119], v[16:23], v112
	v_smfmac_f32_16x16x64_f16 v[220:223], v[116:119], v[64:71], v112
	s_waitcnt lgkmcnt(1)
	v_smfmac_f32_16x16x64_f16 v[208:211], v[120:123], v[24:31], v112
	v_smfmac_f32_16x16x64_f16 v[220:223], v[120:123], v[72:79], v112
	s_waitcnt lgkmcnt(0)
	v_smfmac_f32_16x16x64_f16 v[208:211], v[124:127], v[80:87], v112
	ds_read_b32 v136, v163 offset:15360
	v_smfmac_f32_16x16x64_f16 v[220:223], v[124:127], v[88:95], v112
	ds_read_b32 v148, v165 offset:15360
	v_smfmac_f32_16x16x64_f16 v[216:219], v[116:119], v[48:55], v112
	ds_read_b32 v140, v164 offset:15360
	ds_read_b32 v152, v166 offset:15360
	v_mov_b32_e32 v144, v113
	v_smfmac_f32_16x16x64_f16 v[212:215], v[116:119], v[32:39], v112
	v_mov_b32_e32 v137, 0
	v_mov_b32_e32 v141, 0
	v_mov_b32_e32 v145, 0
	v_mov_b32_e32 v149, 0
	global_store_dword v[170:171], v161, off
	v_lshl_add_u64 v[170:171], v[170:171], 0, s[20:21]
	v_add_f32_e32 v156, v220, v221
	v_add_f32_e32 v159, v208, v209
	v_smfmac_f32_16x16x64_f16 v[216:219], v[120:123], v[56:63], v112
	v_add_f32_e32 v97, v210, v211
	v_add_f32_e32 v98, v222, v223
	v_mov_b32_dpp v159, v156 quad_perm:[0,1,2,3] row_mask:0x2 bank_mask:0xf
	v_exp_f32_e32 v159, v159
	v_smfmac_f32_16x16x64_f16 v[212:215], v[120:123], v[40:47], v112
	v_mov_b32_e32 v138, 0
	v_mov_b32_e32 v139, 0
	v_mov_b32_e32 v150, 0
	v_mov_b32_e32 v151, 0
	v_add_f32_e32 v159, 1.0, v159
	v_rcp_f32_e32 v159, v159
	s_nop 0
	v_add_f32_e32 v155, v216, v217
	v_add_f32_e32 v155, v155, v98
	v_mov_b32_dpp v155, v156 row_shl:6 row_mask:0x2 bank_mask:0xf
	v_fmac_f32_e32 v224, v159, v155
	v_exp_f32_e32 v224, v224
	v_add_f32_e32 v160, v212, v213
	v_add_f32_e32 v160, v160, v97
	v_mov_b32_dpp v160, v156 row_shl:3 row_mask:0x2 bank_mask:0xf
	v_add_f32_e32 v224, 1.0, v224
	v_rcp_f32_e32 v159, v224
	v_exp_f32_e32 v160, v160
	v_fma_f32 v159, v159, -2.0, 1.0
	v_add_f32_e32 v160, 1.0, v160
	v_rcp_f32_e32 v160, v160
	v_sub_f32_e32 v153, v161, v159
	v_fma_f32 v161, v160, v153, v159
	v_fma_mixlo_f16 v162, v160, v153, v159
	ds_write_b16 v168, v162 offset:0
	s_waitcnt lgkmcnt(0)
	s_barrier
	ds_read_b128 v[116:119], v167 offset:0
	ds_read_b128 v[120:123], v167 offset:128
	ds_read_b128 v[124:127], v96 offset:0
	s_waitcnt lgkmcnt(2)
	v_smfmac_f32_16x16x64_f16 v[136:139], v[116:119], v[16:23], v112
	v_smfmac_f32_16x16x64_f16 v[148:151], v[116:119], v[64:71], v112
	s_waitcnt lgkmcnt(1)
	v_smfmac_f32_16x16x64_f16 v[136:139], v[120:123], v[24:31], v112
	v_smfmac_f32_16x16x64_f16 v[148:151], v[120:123], v[72:79], v112
	s_waitcnt lgkmcnt(0)
	v_smfmac_f32_16x16x64_f16 v[136:139], v[124:127], v[80:87], v112
	ds_read_b32 v208, v163 offset:17280
	v_smfmac_f32_16x16x64_f16 v[148:151], v[124:127], v[88:95], v112
	ds_read_b32 v220, v165 offset:17280
	v_smfmac_f32_16x16x64_f16 v[144:147], v[116:119], v[48:55], v112
	ds_read_b32 v212, v164 offset:17280
	ds_read_b32 v224, v166 offset:17280
	v_mov_b32_e32 v216, v113
	v_smfmac_f32_16x16x64_f16 v[140:143], v[116:119], v[32:39], v112
	v_mov_b32_e32 v209, 0
	v_mov_b32_e32 v213, 0
	v_mov_b32_e32 v217, 0
	v_mov_b32_e32 v221, 0
	global_store_dword v[170:171], v161, off
	v_lshl_add_u64 v[170:171], v[170:171], 0, s[20:21]
	v_add_f32_e32 v156, v148, v149
	v_add_f32_e32 v159, v136, v137
	v_smfmac_f32_16x16x64_f16 v[144:147], v[120:123], v[56:63], v112
	v_add_f32_e32 v97, v138, v139
	v_add_f32_e32 v98, v150, v151
	v_mov_b32_dpp v159, v156 quad_perm:[0,1,2,3] row_mask:0x2 bank_mask:0xf
	v_exp_f32_e32 v159, v159
	v_smfmac_f32_16x16x64_f16 v[140:143], v[120:123], v[40:47], v112
	v_mov_b32_e32 v210, 0
	v_mov_b32_e32 v211, 0
	v_mov_b32_e32 v222, 0
	v_mov_b32_e32 v223, 0
	v_add_f32_e32 v159, 1.0, v159
	v_rcp_f32_e32 v159, v159
	s_nop 0
	v_add_f32_e32 v155, v144, v145
	v_add_f32_e32 v155, v155, v98
	v_mov_b32_dpp v155, v156 row_shl:6 row_mask:0x2 bank_mask:0xf
	v_fmac_f32_e32 v152, v159, v155
	v_exp_f32_e32 v152, v152
	v_add_f32_e32 v160, v140, v141
	v_add_f32_e32 v160, v160, v97
	v_mov_b32_dpp v160, v156 row_shl:3 row_mask:0x2 bank_mask:0xf
	v_add_f32_e32 v152, 1.0, v152
	v_rcp_f32_e32 v159, v152
	v_exp_f32_e32 v160, v160
	v_fma_f32 v159, v159, -2.0, 1.0
	v_add_f32_e32 v160, 1.0, v160
	v_rcp_f32_e32 v160, v160
	v_sub_f32_e32 v153, v161, v159
	v_fma_f32 v161, v160, v153, v159
	v_fma_mixlo_f16 v162, v160, v153, v159
	ds_write_b16 v168, v162 offset:384
	s_waitcnt lgkmcnt(0)
	s_barrier
	ds_read_b128 v[116:119], v167 offset:384
	ds_read_b128 v[120:123], v167 offset:512
	ds_read_b128 v[124:127], v96 offset:384
	s_waitcnt lgkmcnt(2)
	v_smfmac_f32_16x16x64_f16 v[208:211], v[116:119], v[16:23], v112
	v_smfmac_f32_16x16x64_f16 v[220:223], v[116:119], v[64:71], v112
	s_waitcnt lgkmcnt(1)
	v_smfmac_f32_16x16x64_f16 v[208:211], v[120:123], v[24:31], v112
	v_smfmac_f32_16x16x64_f16 v[220:223], v[120:123], v[72:79], v112
	s_waitcnt lgkmcnt(0)
	v_smfmac_f32_16x16x64_f16 v[208:211], v[124:127], v[80:87], v112
	ds_read_b32 v136, v163 offset:19200
	v_smfmac_f32_16x16x64_f16 v[220:223], v[124:127], v[88:95], v112
	ds_read_b32 v148, v165 offset:19200
	s_cmp_eq_u32 s26, 7
	s_cbranch_scc1 .Lgru1_nost0
	s_waitcnt vmcnt(4)
	v_mul_f32_e32 v176, s51, v176
	v_mul_f32_e32 v177, s51, v177
	v_mul_f32_e32 v178, s51, v178
	v_mul_f32_e32 v179, s51, v179
	v_mul_f32_e32 v180, v175, v180
	v_mul_f32_e32 v181, v175, v181
	v_mul_f32_e32 v182, s52, v182
	v_mul_f32_e32 v183, s52, v183
	ds_write_b64 v173, v[176:177] offset:0
	ds_write_b64 v173, v[178:179] offset:512
	ds_write_b64 v173, v[180:181] offset:1024
	ds_write_b64 v115, v[182:183] offset:1536
.Lgru1_nost0:
	v_smfmac_f32_16x16x64_f16 v[216:219], v[116:119], v[48:55], v112
	ds_read_b32 v140, v164 offset:19200
	ds_read_b32 v152, v166 offset:19200
	v_mov_b32_e32 v144, v113
	v_smfmac_f32_16x16x64_f16 v[212:215], v[116:119], v[32:39], v112
	v_mov_b32_e32 v137, 0
	v_mov_b32_e32 v141, 0
	v_mov_b32_e32 v145, 0
	v_mov_b32_e32 v149, 0
	global_store_dword v[170:171], v161, off
	v_lshl_add_u64 v[170:171], v[170:171], 0, s[20:21]
	v_add_f32_e32 v156, v220, v221
	v_add_f32_e32 v159, v208, v209
	v_smfmac_f32_16x16x64_f16 v[216:219], v[120:123], v[56:63], v112
	v_add_f32_e32 v97, v210, v211
	v_add_f32_e32 v98, v222, v223
	v_mov_b32_dpp v159, v156 quad_perm:[0,1,2,3] row_mask:0x2 bank_mask:0xf
	v_exp_f32_e32 v159, v159
	v_smfmac_f32_16x16x64_f16 v[212:215], v[120:123], v[40:47], v112
	v_mov_b32_e32 v138, 0
	v_mov_b32_e32 v139, 0
	v_mov_b32_e32 v150, 0
	v_mov_b32_e32 v151, 0
	v_add_f32_e32 v159, 1.0, v159
	v_rcp_f32_e32 v159, v159
	s_nop 0
	v_add_f32_e32 v155, v216, v217
	v_add_f32_e32 v155, v155, v98
	v_mov_b32_dpp v155, v156 row_shl:6 row_mask:0x2 bank_mask:0xf
	v_fmac_f32_e32 v224, v159, v155
	v_exp_f32_e32 v224, v224
	v_add_f32_e32 v160, v212, v213
	v_add_f32_e32 v160, v160, v97
	v_mov_b32_dpp v160, v156 row_shl:3 row_mask:0x2 bank_mask:0xf
	v_add_f32_e32 v224, 1.0, v224
	v_rcp_f32_e32 v159, v224
	v_exp_f32_e32 v160, v160
	v_fma_f32 v159, v159, -2.0, 1.0
	v_add_f32_e32 v160, 1.0, v160
	v_rcp_f32_e32 v160, v160
	v_sub_f32_e32 v153, v161, v159
	v_fma_f32 v161, v160, v153, v159
	v_fma_mixlo_f16 v162, v160, v153, v159
	ds_write_b16 v168, v162 offset:0
	s_waitcnt lgkmcnt(0)
	s_barrier
	ds_read_b128 v[116:119], v167 offset:0
	ds_read_b128 v[120:123], v167 offset:128
	ds_read_b128 v[124:127], v96 offset:0
	s_waitcnt lgkmcnt(2)
	v_smfmac_f32_16x16x64_f16 v[136:139], v[116:119], v[16:23], v112
	v_smfmac_f32_16x16x64_f16 v[148:151], v[116:119], v[64:71], v112
	s_waitcnt lgkmcnt(1)
	v_smfmac_f32_16x16x64_f16 v[136:139], v[120:123], v[24:31], v112
	v_smfmac_f32_16x16x64_f16 v[148:151], v[120:123], v[72:79], v112
	s_waitcnt lgkmcnt(0)
	v_smfmac_f32_16x16x64_f16 v[136:139], v[124:127], v[80:87], v112
	ds_read_b32 v208, v163 offset:21120
	v_smfmac_f32_16x16x64_f16 v[148:151], v[124:127], v[88:95], v112
	ds_read_b32 v220, v165 offset:21120
	v_smfmac_f32_16x16x64_f16 v[144:147], v[116:119], v[48:55], v112
	ds_read_b32 v212, v164 offset:21120
	ds_read_b32 v224, v166 offset:21120
	v_mov_b32_e32 v216, v113
	v_smfmac_f32_16x16x64_f16 v[140:143], v[116:119], v[32:39], v112
	v_mov_b32_e32 v209, 0
	v_mov_b32_e32 v213, 0
	v_mov_b32_e32 v217, 0
	v_mov_b32_e32 v221, 0
	global_store_dword v[170:171], v161, off
	v_lshl_add_u64 v[170:171], v[170:171], 0, s[20:21]
	v_add_f32_e32 v156, v148, v149
	v_add_f32_e32 v159, v136, v137
	v_smfmac_f32_16x16x64_f16 v[144:147], v[120:123], v[56:63], v112
	v_add_f32_e32 v97, v138, v139
	v_add_f32_e32 v98, v150, v151
	v_mov_b32_dpp v159, v156 quad_perm:[0,1,2,3] row_mask:0x2 bank_mask:0xf
	v_exp_f32_e32 v159, v159
	v_smfmac_f32_16x16x64_f16 v[140:143], v[120:123], v[40:47], v112
	v_mov_b32_e32 v210, 0
	v_mov_b32_e32 v211, 0
	v_mov_b32_e32 v222, 0
	v_mov_b32_e32 v223, 0
	v_add_f32_e32 v159, 1.0, v159
	v_rcp_f32_e32 v159, v159
	s_nop 0
	v_add_f32_e32 v155, v144, v145
	v_add_f32_e32 v155, v155, v98
	v_mov_b32_dpp v155, v156 row_shl:6 row_mask:0x2 bank_mask:0xf
	v_fmac_f32_e32 v152, v159, v155
	v_exp_f32_e32 v152, v152
	v_add_f32_e32 v160, v140, v141
	v_add_f32_e32 v160, v160, v97
	v_mov_b32_dpp v160, v156 row_shl:3 row_mask:0x2 bank_mask:0xf
	v_add_f32_e32 v152, 1.0, v152
	v_rcp_f32_e32 v159, v152
	v_exp_f32_e32 v160, v160
	v_fma_f32 v159, v159, -2.0, 1.0
	v_add_f32_e32 v160, 1.0, v160
	v_rcp_f32_e32 v160, v160
	v_sub_f32_e32 v153, v161, v159
	v_fma_f32 v161, v160, v153, v159
	v_fma_mixlo_f16 v162, v160, v153, v159
	ds_write_b16 v168, v162 offset:384
	s_waitcnt lgkmcnt(0)
	s_barrier
	ds_read_b128 v[116:119], v167 offset:384
	ds_read_b128 v[120:123], v167 offset:512
	ds_read_b128 v[124:127], v96 offset:384
	s_waitcnt lgkmcnt(2)
	v_smfmac_f32_16x16x64_f16 v[208:211], v[116:119], v[16:23], v112
	v_smfmac_f32_16x16x64_f16 v[220:223], v[116:119], v[64:71], v112
	s_waitcnt lgkmcnt(1)
	v_smfmac_f32_16x16x64_f16 v[208:211], v[120:123], v[24:31], v112
	v_smfmac_f32_16x16x64_f16 v[220:223], v[120:123], v[72:79], v112
	s_waitcnt lgkmcnt(0)
	v_smfmac_f32_16x16x64_f16 v[208:211], v[124:127], v[80:87], v112
	ds_read_b32 v136, v163 offset:23040
	v_smfmac_f32_16x16x64_f16 v[220:223], v[124:127], v[88:95], v112
	ds_read_b32 v148, v165 offset:23040
	s_cmp_eq_u32 s26, 7
	s_cbranch_scc1 .Lgru1_nost1
	s_waitcnt vmcnt(4)
	v_mul_f32_e32 v184, s51, v184
	v_mul_f32_e32 v185, s51, v185
	v_mul_f32_e32 v186, s51, v186
	v_mul_f32_e32 v187, s51, v187
	v_mul_f32_e32 v188, v175, v188
	v_mul_f32_e32 v189, v175, v189
	v_mul_f32_e32 v190, s52, v190
	v_mul_f32_e32 v191, s52, v191
	ds_write_b64 v174, v[184:185] offset:0
	ds_write_b64 v174, v[186:187] offset:512
	ds_write_b64 v174, v[188:189] offset:1024
	ds_write_b64 v169, v[190:191] offset:1536
.Lgru1_nost1:
	v_smfmac_f32_16x16x64_f16 v[216:219], v[116:119], v[48:55], v112
	ds_read_b32 v140, v164 offset:23040
	ds_read_b32 v152, v166 offset:23040
	v_mov_b32_e32 v144, v113
	v_smfmac_f32_16x16x64_f16 v[212:215], v[116:119], v[32:39], v112
	v_mov_b32_e32 v137, 0
	v_mov_b32_e32 v141, 0
	v_mov_b32_e32 v145, 0
	v_mov_b32_e32 v149, 0
	global_store_dword v[170:171], v161, off
	v_lshl_add_u64 v[170:171], v[170:171], 0, s[20:21]
	v_add_f32_e32 v156, v220, v221
	v_add_f32_e32 v159, v208, v209
	v_smfmac_f32_16x16x64_f16 v[216:219], v[120:123], v[56:63], v112
	v_add_f32_e32 v97, v210, v211
	v_add_f32_e32 v98, v222, v223
	v_mov_b32_dpp v159, v156 quad_perm:[0,1,2,3] row_mask:0x2 bank_mask:0xf
	v_exp_f32_e32 v159, v159
	v_smfmac_f32_16x16x64_f16 v[212:215], v[120:123], v[40:47], v112
	v_mov_b32_e32 v138, 0
	v_mov_b32_e32 v139, 0
	v_mov_b32_e32 v150, 0
	v_mov_b32_e32 v151, 0
	v_add_f32_e32 v159, 1.0, v159
	v_rcp_f32_e32 v159, v159
	s_nop 0
	v_add_f32_e32 v155, v216, v217
	v_add_f32_e32 v155, v155, v98
	v_mov_b32_dpp v155, v156 row_shl:6 row_mask:0x2 bank_mask:0xf
	v_fmac_f32_e32 v224, v159, v155
	v_exp_f32_e32 v224, v224
	v_add_f32_e32 v160, v212, v213
	v_add_f32_e32 v160, v160, v97
	v_mov_b32_dpp v160, v156 row_shl:3 row_mask:0x2 bank_mask:0xf
	v_add_f32_e32 v224, 1.0, v224
	v_rcp_f32_e32 v159, v224
	v_exp_f32_e32 v160, v160
	v_fma_f32 v159, v159, -2.0, 1.0
	v_add_f32_e32 v160, 1.0, v160
	v_rcp_f32_e32 v160, v160
	v_sub_f32_e32 v153, v161, v159
	v_fma_f32 v161, v160, v153, v159
	v_fma_mixlo_f16 v162, v160, v153, v159
	ds_write_b16 v168, v162 offset:0
	s_waitcnt lgkmcnt(0)
	s_barrier
	ds_read_b128 v[116:119], v167 offset:0
	ds_read_b128 v[120:123], v167 offset:128
	ds_read_b128 v[124:127], v96 offset:0
	s_waitcnt lgkmcnt(2)
	v_smfmac_f32_16x16x64_f16 v[136:139], v[116:119], v[16:23], v112
	v_smfmac_f32_16x16x64_f16 v[148:151], v[116:119], v[64:71], v112
	s_waitcnt lgkmcnt(1)
	v_smfmac_f32_16x16x64_f16 v[136:139], v[120:123], v[24:31], v112
	v_smfmac_f32_16x16x64_f16 v[148:151], v[120:123], v[72:79], v112
	s_waitcnt lgkmcnt(0)
	v_smfmac_f32_16x16x64_f16 v[136:139], v[124:127], v[80:87], v112
	ds_read_b32 v208, v163 offset:24960
	v_smfmac_f32_16x16x64_f16 v[148:151], v[124:127], v[88:95], v112
	ds_read_b32 v220, v165 offset:24960
	v_smfmac_f32_16x16x64_f16 v[144:147], v[116:119], v[48:55], v112
	ds_read_b32 v212, v164 offset:24960
	ds_read_b32 v224, v166 offset:24960
	v_mov_b32_e32 v216, v113
	v_smfmac_f32_16x16x64_f16 v[140:143], v[116:119], v[32:39], v112
	v_mov_b32_e32 v209, 0
	v_mov_b32_e32 v213, 0
	v_mov_b32_e32 v217, 0
	v_mov_b32_e32 v221, 0
	global_store_dword v[170:171], v161, off
	v_lshl_add_u64 v[170:171], v[170:171], 0, s[20:21]
	v_add_f32_e32 v156, v148, v149
	v_add_f32_e32 v159, v136, v137
	v_smfmac_f32_16x16x64_f16 v[144:147], v[120:123], v[56:63], v112
	v_add_f32_e32 v97, v138, v139
	v_add_f32_e32 v98, v150, v151
	v_mov_b32_dpp v159, v156 quad_perm:[0,1,2,3] row_mask:0x2 bank_mask:0xf
	v_exp_f32_e32 v159, v159
	v_smfmac_f32_16x16x64_f16 v[140:143], v[120:123], v[40:47], v112
	v_mov_b32_e32 v210, 0
	v_mov_b32_e32 v211, 0
	v_mov_b32_e32 v222, 0
	v_mov_b32_e32 v223, 0
	v_add_f32_e32 v159, 1.0, v159
	v_rcp_f32_e32 v159, v159
	s_nop 0
	v_add_f32_e32 v155, v144, v145
	v_add_f32_e32 v155, v155, v98
	v_mov_b32_dpp v155, v156 row_shl:6 row_mask:0x2 bank_mask:0xf
	v_fmac_f32_e32 v152, v159, v155
	v_exp_f32_e32 v152, v152
	v_add_f32_e32 v160, v140, v141
	v_add_f32_e32 v160, v160, v97
	v_mov_b32_dpp v160, v156 row_shl:3 row_mask:0x2 bank_mask:0xf
	v_add_f32_e32 v152, 1.0, v152
	v_rcp_f32_e32 v159, v152
	v_exp_f32_e32 v160, v160
	v_fma_f32 v159, v159, -2.0, 1.0
	v_add_f32_e32 v160, 1.0, v160
	v_rcp_f32_e32 v160, v160
	v_sub_f32_e32 v153, v161, v159
	v_fma_f32 v161, v160, v153, v159
	v_fma_mixlo_f16 v162, v160, v153, v159
	ds_write_b16 v168, v162 offset:384
	s_waitcnt lgkmcnt(0)
	s_barrier
	ds_read_b128 v[116:119], v167 offset:384
	ds_read_b128 v[120:123], v167 offset:512
	ds_read_b128 v[124:127], v96 offset:384
	s_waitcnt lgkmcnt(2)
	v_smfmac_f32_16x16x64_f16 v[208:211], v[116:119], v[16:23], v112
	v_smfmac_f32_16x16x64_f16 v[220:223], v[116:119], v[64:71], v112
	s_waitcnt lgkmcnt(1)
	v_smfmac_f32_16x16x64_f16 v[208:211], v[120:123], v[24:31], v112
	v_smfmac_f32_16x16x64_f16 v[220:223], v[120:123], v[72:79], v112
	s_waitcnt lgkmcnt(0)
	v_smfmac_f32_16x16x64_f16 v[208:211], v[124:127], v[80:87], v112
	ds_read_b32 v136, v163 offset:26880
	v_smfmac_f32_16x16x64_f16 v[220:223], v[124:127], v[88:95], v112
	ds_read_b32 v148, v165 offset:26880
	v_smfmac_f32_16x16x64_f16 v[216:219], v[116:119], v[48:55], v112
	ds_read_b32 v140, v164 offset:26880
	ds_read_b32 v152, v166 offset:26880
	v_mov_b32_e32 v144, v113
	v_smfmac_f32_16x16x64_f16 v[212:215], v[116:119], v[32:39], v112
	v_mov_b32_e32 v137, 0
	v_mov_b32_e32 v141, 0
	v_mov_b32_e32 v145, 0
	v_mov_b32_e32 v149, 0
	global_store_dword v[170:171], v161, off
	v_lshl_add_u64 v[170:171], v[170:171], 0, s[20:21]
	v_add_f32_e32 v156, v220, v221
	v_add_f32_e32 v159, v208, v209
	v_smfmac_f32_16x16x64_f16 v[216:219], v[120:123], v[56:63], v112
	v_add_f32_e32 v97, v210, v211
	v_add_f32_e32 v98, v222, v223
	v_mov_b32_dpp v159, v156 quad_perm:[0,1,2,3] row_mask:0x2 bank_mask:0xf
	v_exp_f32_e32 v159, v159
	v_smfmac_f32_16x16x64_f16 v[212:215], v[120:123], v[40:47], v112
	v_mov_b32_e32 v138, 0
	v_mov_b32_e32 v139, 0
	v_mov_b32_e32 v150, 0
	v_mov_b32_e32 v151, 0
	v_add_f32_e32 v159, 1.0, v159
	v_rcp_f32_e32 v159, v159
	s_nop 0
	v_add_f32_e32 v155, v216, v217
	v_add_f32_e32 v155, v155, v98
	v_mov_b32_dpp v155, v156 row_shl:6 row_mask:0x2 bank_mask:0xf
	v_fmac_f32_e32 v224, v159, v155
	v_exp_f32_e32 v224, v224
	v_add_f32_e32 v160, v212, v213
	v_add_f32_e32 v160, v160, v97
	v_mov_b32_dpp v160, v156 row_shl:3 row_mask:0x2 bank_mask:0xf
	v_add_f32_e32 v224, 1.0, v224
	v_rcp_f32_e32 v159, v224
	v_exp_f32_e32 v160, v160
	v_fma_f32 v159, v159, -2.0, 1.0
	v_add_f32_e32 v160, 1.0, v160
	v_rcp_f32_e32 v160, v160
	v_sub_f32_e32 v153, v161, v159
	v_fma_f32 v161, v160, v153, v159
	v_fma_mixlo_f16 v162, v160, v153, v159
	ds_write_b16 v168, v162 offset:0
	s_waitcnt lgkmcnt(0)
	s_barrier
	ds_read_b128 v[116:119], v167 offset:0
	ds_read_b128 v[120:123], v167 offset:128
	ds_read_b128 v[124:127], v96 offset:0
	s_waitcnt lgkmcnt(2)
	v_smfmac_f32_16x16x64_f16 v[136:139], v[116:119], v[16:23], v112
	v_smfmac_f32_16x16x64_f16 v[148:151], v[116:119], v[64:71], v112
	s_waitcnt lgkmcnt(1)
	v_smfmac_f32_16x16x64_f16 v[136:139], v[120:123], v[24:31], v112
	v_smfmac_f32_16x16x64_f16 v[148:151], v[120:123], v[72:79], v112
	s_waitcnt lgkmcnt(0)
	v_smfmac_f32_16x16x64_f16 v[136:139], v[124:127], v[80:87], v112
	ds_read_b32 v208, v163 offset:28800
	v_smfmac_f32_16x16x64_f16 v[148:151], v[124:127], v[88:95], v112
	ds_read_b32 v220, v165 offset:28800
	v_smfmac_f32_16x16x64_f16 v[144:147], v[116:119], v[48:55], v112
	ds_read_b32 v212, v164 offset:28800
	ds_read_b32 v224, v166 offset:28800
	v_mov_b32_e32 v216, v113
	v_smfmac_f32_16x16x64_f16 v[140:143], v[116:119], v[32:39], v112
	v_mov_b32_e32 v209, 0
	v_mov_b32_e32 v213, 0
	v_mov_b32_e32 v217, 0
	v_mov_b32_e32 v221, 0
	global_store_dword v[170:171], v161, off
	v_lshl_add_u64 v[170:171], v[170:171], 0, s[20:21]
	v_add_f32_e32 v156, v148, v149
	v_add_f32_e32 v159, v136, v137
	v_smfmac_f32_16x16x64_f16 v[144:147], v[120:123], v[56:63], v112
	v_add_f32_e32 v97, v138, v139
	v_add_f32_e32 v98, v150, v151
	v_mov_b32_dpp v159, v156 quad_perm:[0,1,2,3] row_mask:0x2 bank_mask:0xf
	v_exp_f32_e32 v159, v159
	v_smfmac_f32_16x16x64_f16 v[140:143], v[120:123], v[40:47], v112
	v_mov_b32_e32 v210, 0
	v_mov_b32_e32 v211, 0
	v_mov_b32_e32 v222, 0
	v_mov_b32_e32 v223, 0
	v_add_f32_e32 v159, 1.0, v159
	v_rcp_f32_e32 v159, v159
	s_nop 0
	v_add_f32_e32 v155, v144, v145
	v_add_f32_e32 v155, v155, v98
	v_mov_b32_dpp v155, v156 row_shl:6 row_mask:0x2 bank_mask:0xf
	v_fmac_f32_e32 v152, v159, v155
	v_exp_f32_e32 v152, v152
	v_add_f32_e32 v160, v140, v141
	v_add_f32_e32 v160, v160, v97
	v_mov_b32_dpp v160, v156 row_shl:3 row_mask:0x2 bank_mask:0xf
	v_add_f32_e32 v152, 1.0, v152
	v_rcp_f32_e32 v159, v152
	v_exp_f32_e32 v160, v160
	v_fma_f32 v159, v159, -2.0, 1.0
	v_add_f32_e32 v160, 1.0, v160
	v_rcp_f32_e32 v160, v160
	v_sub_f32_e32 v153, v161, v159
	v_fma_f32 v161, v160, v153, v159
	v_fma_mixlo_f16 v162, v160, v153, v159
	ds_write_b16 v168, v162 offset:384
	s_waitcnt lgkmcnt(0)
	s_barrier
	ds_read_b128 v[116:119], v167 offset:384
	ds_read_b128 v[120:123], v167 offset:512
	ds_read_b128 v[124:127], v96 offset:384
	s_waitcnt lgkmcnt(2)
	v_smfmac_f32_16x16x64_f16 v[208:211], v[116:119], v[16:23], v112
	v_smfmac_f32_16x16x64_f16 v[220:223], v[116:119], v[64:71], v112
	s_waitcnt lgkmcnt(1)
	v_smfmac_f32_16x16x64_f16 v[208:211], v[120:123], v[24:31], v112
	v_smfmac_f32_16x16x64_f16 v[220:223], v[120:123], v[72:79], v112
	s_waitcnt lgkmcnt(0)
	v_smfmac_f32_16x16x64_f16 v[208:211], v[124:127], v[80:87], v112
	v_xor_b32_e32 v163, 0x7800, v163
	v_xor_b32_e32 v164, 0x7800, v164
	v_xor_b32_e32 v165, 0x7800, v165
	v_xor_b32_e32 v166, 0x7800, v166
	ds_read_b32 v136, v163 offset:0
	v_smfmac_f32_16x16x64_f16 v[220:223], v[124:127], v[88:95], v112
	ds_read_b32 v148, v165 offset:0
	v_smfmac_f32_16x16x64_f16 v[216:219], v[116:119], v[48:55], v112
	ds_read_b32 v140, v164 offset:0
	ds_read_b32 v152, v166 offset:0
	v_mov_b32_e32 v144, v113
	v_smfmac_f32_16x16x64_f16 v[212:215], v[116:119], v[32:39], v112
	v_mov_b32_e32 v137, 0
	v_mov_b32_e32 v141, 0
	v_mov_b32_e32 v145, 0
	v_mov_b32_e32 v149, 0
	global_store_dword v[170:171], v161, off
	v_lshl_add_u64 v[170:171], v[170:171], 0, s[20:21]
	v_add_f32_e32 v156, v220, v221
	v_add_f32_e32 v159, v208, v209
	v_smfmac_f32_16x16x64_f16 v[216:219], v[120:123], v[56:63], v112
	v_add_f32_e32 v97, v210, v211
	v_add_f32_e32 v98, v222, v223
	v_mov_b32_dpp v159, v156 quad_perm:[0,1,2,3] row_mask:0x2 bank_mask:0xf
	v_exp_f32_e32 v159, v159
	v_smfmac_f32_16x16x64_f16 v[212:215], v[120:123], v[40:47], v112
	v_mov_b32_e32 v138, 0
	v_mov_b32_e32 v139, 0
	v_mov_b32_e32 v150, 0
	v_mov_b32_e32 v151, 0
	v_add_u32_e32 v173, s55, v173
	v_add_u32_e32 v174, s55, v174
	v_add_u32_e32 v115, s55, v115
	v_add_u32_e32 v169, s55, v169
	s_sub_i32 s55, 0, s55
	v_add_f32_e32 v159, 1.0, v159
	v_rcp_f32_e32 v159, v159
	s_nop 0
	v_add_f32_e32 v155, v216, v217
	v_add_f32_e32 v155, v155, v98
	v_mov_b32_dpp v155, v156 row_shl:6 row_mask:0x2 bank_mask:0xf
	v_fmac_f32_e32 v224, v159, v155
	v_exp_f32_e32 v224, v224
	v_add_f32_e32 v160, v212, v213
	v_add_f32_e32 v160, v160, v97
	v_mov_b32_dpp v160, v156 row_shl:3 row_mask:0x2 bank_mask:0xf
	v_add_f32_e32 v224, 1.0, v224
	v_rcp_f32_e32 v159, v224
	v_exp_f32_e32 v160, v160
	v_fma_f32 v159, v159, -2.0, 1.0
	v_add_f32_e32 v160, 1.0, v160
	v_rcp_f32_e32 v160, v160
	v_sub_f32_e32 v153, v161, v159
	v_fma_f32 v161, v160, v153, v159
	v_fma_mixlo_f16 v162, v160, v153, v159
	ds_write_b16 v168, v162 offset:0
	s_waitcnt lgkmcnt(0)
	s_barrier
	s_add_i32 s26, s26, 1
	s_cmp_lt_u32 s26, 8
	s_cbranch_scc1 .Lgru1_chunk
	global_store_dword v[170:171], v161, off
.LBB5_143:
	s_endpgm
	s_nop 0
	s_nop 0
	s_nop 0
	s_nop 0
	s_nop 0
	s_nop 0
	s_nop 0
	s_nop 0
	s_nop 0
	s_nop 0
	s_nop 0
	s_nop 0
	s_nop 0
	s_nop 0
	s_nop 0
	s_nop 0
	s_nop 0
	s_nop 0
	s_nop 0
	s_nop 0
	s_nop 0
	s_nop 0
	s_nop 0
	s_nop 0
	s_nop 0
	s_nop 0
	s_nop 0
	s_nop 0
	s_nop 0
	s_nop 0
	s_nop 0
	s_nop 0
	s_nop 0
	s_nop 0
	s_nop 0
	s_nop 0
	s_nop 0
	s_nop 0
	s_nop 0
	s_endpgm

	.amdhsa_kernel _Z15gru_mfma_kernelILi1EEvPKfmS1_S1_S1_S1_PfS2_i7PreArgs
		.amdhsa_group_segment_fixed_size 63488
		.amdhsa_private_segment_fixed_size 0
		.amdhsa_kernarg_size 448
		.amdhsa_user_sgpr_count 2
		.amdhsa_user_sgpr_dispatch_ptr 0
		.amdhsa_user_sgpr_queue_ptr 0
		.amdhsa_user_sgpr_kernarg_segment_ptr 1
		.amdhsa_user_sgpr_dispatch_id 0
		.amdhsa_user_sgpr_kernarg_preload_length 0
		.amdhsa_user_sgpr_kernarg_preload_offset 0
		.amdhsa_user_sgpr_private_segment_size 0
		.amdhsa_uses_dynamic_stack 0
		.amdhsa_enable_private_segment 0
		.amdhsa_system_sgpr_workgroup_id_x 1
		.amdhsa_system_sgpr_workgroup_id_y 0
		.amdhsa_system_sgpr_workgroup_id_z 0
		.amdhsa_system_sgpr_workgroup_info 0
		.amdhsa_system_vgpr_workitem_id 0
		.amdhsa_next_free_vgpr 232
		.amdhsa_next_free_sgpr 96
		.amdhsa_accum_offset 232
		.amdhsa_reserve_vcc 1
		.amdhsa_float_round_mode_32 0
		.amdhsa_float_round_mode_16_64 0
		.amdhsa_float_denorm_mode_32 3
		.amdhsa_float_denorm_mode_16_64 3
		.amdhsa_dx10_clamp 1
		.amdhsa_ieee_mode 1
		.amdhsa_fp16_overflow 0
		.amdhsa_tg_split 0
		.amdhsa_exception_fp_ieee_invalid_op 0
		.amdhsa_exception_fp_denorm_src 0
		.amdhsa_exception_fp_ieee_div_zero 0
		.amdhsa_exception_fp_ieee_overflow 0
		.amdhsa_exception_fp_ieee_underflow 0
		.amdhsa_exception_fp_ieee_inexact 0
		.amdhsa_exception_int_div_zero 0
	.end_amdhsa_kernel

.LBB6_26:
	s_and_b64 vcc, exec, s[4:5]
	s_cbranch_vccz .LBB6_81
	s_setprio 3
	s_load_dwordx2 s[8:9], s[0:1], 0x0
	s_load_dwordx2 s[10:11], s[0:1], 0x8
	s_load_dwordx2 s[12:13], s[0:1], 0x18
	s_load_dwordx2 s[32:33], s[0:1], 0x28
	s_load_dwordx4 s[36:39], s[0:1], 0x30
	s_load_dwordx2 s[18:19], s[0:1], 0xb8
	s_load_dwordx2 s[16:17], s[0:1], 0xc8
	s_load_dword s34, s[0:1], 0xd4
	s_lshr_b32 s3, s2, 4
	s_bfe_u32 s4, s2, 0x10003
	s_and_b32 s5, s2, 7
	v_lshrrev_b32_e32 v1, 6, v0
	v_and_b32_e32 v2, 63, v0
	v_and_b32_e32 v3, 15, v0
	v_bfe_u32 v4, v0, 4, 2
	s_nop 1
	v_readfirstlane_b32 s6, v1
	s_waitcnt lgkmcnt(0)
	s_cmp_eq_u32 s3, 0
	s_cselect_b32 s12, s12, s32
	s_cselect_b32 s13, s13, s33
	s_cselect_b32 s14, s36, s38
	s_cselect_b32 s15, s37, s39
	s_mul_i32 s35, s4, 0x708
	s_add_u32 s12, s12, s35
	s_addc_u32 s13, s13, 0
	s_mul_i32 s35, s5, 0x25800
	s_add_u32 s14, s14, s35
	s_addc_u32 s15, s15, 0
	s_mul_i32 s35, s4, 0x258
	s_add_u32 s14, s14, s35
	s_addc_u32 s15, s15, 0
	s_lshl_b64 s[10:11], s[10:11], 2
	s_mul_i32 s35, s3, 0x384000
	s_add_u32 s8, s8, s35
	s_addc_u32 s9, s9, 0
	s_mul_i32 s35, s5, 0x70800
	s_add_u32 s8, s8, s35
	s_addc_u32 s9, s9, 0
	s_mul_i32 s35, s4, 0x708
	s_add_u32 s8, s8, s35
	s_addc_u32 s9, s9, 0
	s_mul_i32 s35, s4, 112
	s_lshl_b32 s40, s6, 1
	s_add_i32 s35, s35, s40
	s_mul_i32 s35, s35, 0xe10
	s_add_u32 s22, s8, s35
	s_addc_u32 s23, s9, 0
	s_add_u32 s46, s22, 0xe10
	s_addc_u32 s47, s23, 0
	s_add_u32 s24, s22, s10
	s_addc_u32 s25, s23, s11
	s_add_u32 s48, s24, 0xe10
	s_addc_u32 s49, s25, 0
	s_cmp_eq_u32 s4, 0
	s_mov_b32 s27, 0xffff1f00
	s_mov_b32 s20, 0xfffffb50
	s_cselect_b32 s27, 0xe100, s27
	s_cselect_b32 s50, 0, -1
	s_cselect_b32 s20, 0x4b0, s20
	s_cselect_b32 s21, 0, -1
	s_lshl_b32 s35, s3, 1
	s_add_i32 s35, s35, s4
	s_add_i32 s35, s35, s34
	s_mul_i32 s35, s35, 0x28000
	s_add_u32 s16, s16, s35
	s_addc_u32 s17, s17, 0
	s_mul_i32 s35, s6, 0x5000
	s_add_u32 s16, s16, s35
	s_addc_u32 s17, s17, 0
	s_mov_b32 s28, 0xffff
	s_mov_b32 s29, 0
	s_mov_b32 s30, -1
	s_mov_b32 s31, 1
	s_mov_b32 s68, 0x00330033
	s_mov_b32 s69, 0x00330033
	s_mov_b32 s51, 0xbfb8aa3b
	s_mov_b32 s52, 0x4038aa3b
	v_lshlrev_b32_e32 v5, 4, v2
	s_add_u32 s42, s16, 0x0
	s_addc_u32 s43, s17, 0
	global_load_dwordx4 v[16:19], v5, s[42:43] offset:0
	global_load_dwordx4 v[20:23], v5, s[42:43] offset:1024
	global_load_dwordx4 v[24:27], v5, s[42:43] offset:2048
	global_load_dwordx4 v[28:31], v5, s[42:43] offset:3072
	s_add_u32 s42, s16, 0x1000
	s_addc_u32 s43, s17, 0
	global_load_dwordx4 v[80:83], v5, s[42:43]
	s_add_u32 s42, s16, 0x1400
	s_addc_u32 s43, s17, 0
	global_load_dwordx4 v[32:35], v5, s[42:43] offset:0
	global_load_dwordx4 v[36:39], v5, s[42:43] offset:1024
	global_load_dwordx4 v[40:43], v5, s[42:43] offset:2048
	global_load_dwordx4 v[44:47], v5, s[42:43] offset:3072
	s_add_u32 s42, s16, 0x2400
	s_addc_u32 s43, s17, 0
	global_load_dwordx4 v[84:87], v5, s[42:43]
	s_add_u32 s42, s16, 0x2800
	s_addc_u32 s43, s17, 0
	global_load_dwordx4 v[48:51], v5, s[42:43] offset:0
	global_load_dwordx4 v[52:55], v5, s[42:43] offset:1024
	global_load_dwordx4 v[56:59], v5, s[42:43] offset:2048
	global_load_dwordx4 v[60:63], v5, s[42:43] offset:3072
	s_add_u32 s42, s16, 0x3800
	s_addc_u32 s43, s17, 0
	global_load_dwordx4 v[92:95], v5, s[42:43]
	s_add_u32 s42, s16, 0x3c00
	s_addc_u32 s43, s17, 0
	global_load_dwordx4 v[64:67], v5, s[42:43] offset:0
	global_load_dwordx4 v[68:71], v5, s[42:43] offset:1024
	global_load_dwordx4 v[72:75], v5, s[42:43] offset:2048
	global_load_dwordx4 v[76:79], v5, s[42:43] offset:3072
	s_add_u32 s42, s16, 0x4c00
	s_addc_u32 s43, s17, 0
	global_load_dwordx4 v[88:91], v5, s[42:43]
	v_lshlrev_b32_e32 v172, 3, v2
	v_min_u32_e32 v6, 32, v2
	v_lshlrev_b32_e32 v114, 3, v6
	global_load_dwordx2 v[176:177], v172, s[22:23] offset:0
	global_load_dwordx2 v[178:179], v172, s[22:23] offset:512
	global_load_dwordx2 v[180:181], v172, s[22:23] offset:1024
	global_load_dwordx2 v[182:183], v114, s[22:23] offset:1536
	global_load_dwordx2 v[192:193], v172, s[24:25] offset:0
	global_load_dwordx2 v[194:195], v172, s[24:25] offset:512
	global_load_dwordx2 v[196:197], v172, s[24:25] offset:1024
	global_load_dwordx2 v[198:199], v114, s[24:25] offset:1536
	global_load_dwordx2 v[184:185], v172, s[46:47] offset:0
	global_load_dwordx2 v[186:187], v172, s[46:47] offset:512
	global_load_dwordx2 v[188:189], v172, s[46:47] offset:1024
	global_load_dwordx2 v[190:191], v114, s[46:47] offset:1536
	global_load_dwordx2 v[200:201], v172, s[48:49] offset:0
	global_load_dwordx2 v[202:203], v172, s[48:49] offset:512
	global_load_dwordx2 v[204:205], v172, s[48:49] offset:1024
	global_load_dwordx2 v[206:207], v114, s[48:49] offset:1536
	v_and_b32_e32 v6, 1, v3
	v_cmp_eq_u32_e32 vcc, 1, v6
	v_mov_b32_e32 v7, 0x44444444
	v_mov_b32_e32 v8, 0xeeeeeeee
	s_nop 1
	v_cndmask_b32_e32 v112, v7, v8, vcc
	s_mul_i32 s53, s6, 19
	v_add_u32_e32 v6, s53, v3
	v_cmp_gt_u32_e32 vcc, 0x96, v6
	v_add_u32_e32 v7, 0x12c, v6
	v_mov_b32_e32 v8, 0x12c
	s_nop 1
	v_cndmask_b32_e32 v7, v8, v7, vcc
	v_lshlrev_b32_e32 v7, 2, v7
	global_load_dword v9, v7, s[12:13]
	s_mov_b64 s[54:55], vcc
	v_cmp_gt_u32_e32 vcc, 0xc0, v0
	v_lshlrev_b32_e32 v10, 2, v0
	v_mov_b32_e32 v11, 0
	s_and_saveexec_b64 s[44:45], vcc
	ds_write_b32 v10, v11 offset:61440
	s_mov_b64 exec, s[44:45]
	v_and_b32_e32 v10, 31, v0
	v_lshrrev_b32_e32 v11, 5, v0
	v_subrev_u32_e32 v12, 6, v10
	v_max_i32_e32 v12, 0, v12
	v_mul_u32_u24_e32 v13, 11, v12
	v_lshrrev_b32_e32 v13, 5, v13
	v_mul_u32_u24_e32 v14, 3, v13
	v_sub_u32_e32 v14, v12, v14
	v_mul_u32_u24_e32 v15, 19, v13
	v_add3_u32 v15, v15, v14, 16
	v_cmp_gt_u32_e32 vcc, 0x96, v15
	v_cmp_lt_u32_e64 s[56:57], 5, v10
	v_cmp_gt_u32_e64 s[58:59], 30, v10
	s_and_b64 s[56:57], s[56:57], vcc
	s_and_b64 s[56:57], s[56:57], s[58:59]
	v_add_u32_e32 v15, 0x12c, v15
	v_mov_b32_e32 v14, 0x12c
	v_cndmask_b32_e64 v15, v14, v15, s[56:57]
	v_lshlrev_b32_e32 v15, 2, v15
	global_load_dword v14, v15, s[12:13]
	v_mul_u32_u24_e32 v11, 0x780, v11
	v_lshl_add_u32 v11, v10, 2, v11
	s_waitcnt vmcnt(0)
	v_mul_f32_e32 v14, s52, v14
	v_mul_f32_e32 v9, s52, v9
	v_cndmask_b32_e64 v14, 0, v14, s[56:57]
	v_cndmask_b32_e64 v113, 0, v9, s[54:55]
	s_and_saveexec_b64 s[44:45], s[58:59]
	ds_write_b32 v11, v14 offset:1800
	ds_write_b32 v11, v14 offset:32520
	s_mov_b64 exec, s[44:45]
	v_lshlrev_b32_e32 v172, 3, v2
	s_lshl_b32 s35, s6, 1
	s_sub_i32 s40, 15, s35
	s_cmp_eq_u32 s4, 0
	s_cselect_b32 s41, s35, s40
	s_add_i32 s35, s35, 1
	s_sub_i32 s40, 15, s35
	s_cmp_eq_u32 s4, 0
	s_cselect_b32 s40, s35, s40
	s_mul_i32 s41, s41, 0x780
	s_mul_i32 s40, s40, 0x780
	v_add_u32_e32 v173, s41, v172
	v_add_u32_e32 v174, s40, v172
	v_min_u32_e32 v6, 32, v2
	v_lshlrev_b32_e32 v114, 3, v6
	v_add_u32_e32 v115, s41, v114
	v_add_u32_e32 v169, s40, v114
	v_cmp_lt_u32_e32 vcc, 21, v2
	v_mov_b32_e32 v6, s51
	v_mov_b32_e32 v7, s52
	s_nop 0
	v_cndmask_b32_e32 v175, v6, v7, vcc
	s_waitcnt vmcnt(0)
	v_add_f32_e32 v176, v176, v192
	v_add_f32_e32 v177, v177, v193
	v_mul_f32_e32 v176, s51, v176
	v_mul_f32_e32 v177, s51, v177
	v_add_f32_e32 v178, v178, v194
	v_add_f32_e32 v179, v179, v195
	v_mul_f32_e32 v178, s51, v178
	v_mul_f32_e32 v179, s51, v179
	v_add_f32_e32 v180, v180, v196
	v_add_f32_e32 v181, v181, v197
	v_mul_f32_e32 v180, v175, v180
	v_mul_f32_e32 v181, v175, v181
	v_add_f32_e32 v182, v182, v198
	v_add_f32_e32 v183, v183, v199
	v_mul_f32_e32 v182, s52, v182
	v_mul_f32_e32 v183, s52, v183
	ds_write_b64 v173, v[176:177] offset:0
	ds_write_b64 v173, v[178:179] offset:512
	ds_write_b64 v173, v[180:181] offset:1024
	ds_write_b64 v115, v[182:183] offset:1536
	v_add_f32_e32 v184, v184, v200
	v_add_f32_e32 v185, v185, v201
	v_mul_f32_e32 v184, s51, v184
	v_mul_f32_e32 v185, s51, v185
	v_add_f32_e32 v186, v186, v202
	v_add_f32_e32 v187, v187, v203
	v_mul_f32_e32 v186, s51, v186
	v_mul_f32_e32 v187, s51, v187
	v_add_f32_e32 v188, v188, v204
	v_add_f32_e32 v189, v189, v205
	v_mul_f32_e32 v188, v175, v188
	v_mul_f32_e32 v189, v175, v189
	v_add_f32_e32 v190, v190, v206
	v_add_f32_e32 v191, v191, v207
	v_mul_f32_e32 v190, s52, v190
	v_mul_f32_e32 v191, s52, v191
	ds_write_b64 v174, v[184:185] offset:0
	ds_write_b64 v174, v[186:187] offset:512
	ds_write_b64 v174, v[188:189] offset:1024
	ds_write_b64 v169, v[190:191] offset:1536
	s_movk_i32 s55, 0x7800
	v_add_u32_e32 v173, s55, v173
	v_add_u32_e32 v174, s55, v174
	v_add_u32_e32 v115, s55, v115
	v_add_u32_e32 v169, s55, v169
	s_sub_i32 s55, 0, s55
	v_add_u32_e32 v6, s53, v2
	v_cmp_gt_u32_e32 vcc, 0x96, v6
	v_cmp_gt_u32_e64 s[56:57], 16, v2
	v_cmp_gt_u32_e64 s[58:59], 19, v2
	s_and_b64 s[56:57], s[56:57], vcc
	s_and_b64 s[58:59], s[58:59], vcc
	v_mov_b32_e32 v7, 0x710
	v_lshlrev_b32_e32 v8, 2, v6
	v_add_u32_e32 v9, 0x258, v8
	v_add_u32_e32 v10, 0x4b0, v8
	v_cndmask_b32_e64 v163, v7, v8, s[56:57]
	v_cndmask_b32_e64 v164, v7, v9, s[56:57]
	v_cndmask_b32_e64 v166, v7, v10, s[58:59]
	v_subrev_u32_e32 v9, 16, v2
	v_cmp_gt_u32_e64 s[60:61], 6, v9
	v_cmp_lt_u32_e32 vcc, 2, v9
	v_mov_b32_e32 v11, 0x93
	s_nop 0
	v_cndmask_b32_e32 v10, 0, v11, vcc
	v_cndmask_b32_e64 v12, 0, 3, vcc
	v_sub_u32_e32 v13, v6, v12
	v_cmp_gt_u32_e32 vcc, 0x96, v13
	s_and_b64 s[60:61], s[60:61], vcc
	v_add_u32_e32 v13, v6, v10
	v_lshlrev_b32_e32 v13, 2, v13
	v_cndmask_b32_e64 v165, v7, v13, s[60:61]
	v_subrev_u32_e32 v9, 22, v2
	v_cmp_gt_u32_e32 vcc, 3, v9
	s_mul_i32 s35, s6, 3
	s_addk_i32 s35, 0x1c8
	v_add_lshl_u32 v9, v9, s35, 2
	s_nop 0
	v_cndmask_b32_e32 v165, v165, v9, vcc
	v_and_b32_e32 v9, 1, v3
	v_lshlrev_b32_e32 v9, 4, v9
	v_lshl_or_b32 v9, v4, 5, v9
	v_add_u32_e32 v167, 0xf000, v9
	v_and_b32_e32 v9, 0xfffffff0, v6
	v_bfe_u32 v10, v6, 1, 1
	v_lshl_or_b32 v9, v10, 3, v9
	v_bfe_u32 v10, v6, 2, 2
	v_lshl_or_b32 v9, v10, 1, v9
	v_and_b32_e32 v10, 1, v6
	v_or_b32_e32 v9, v9, v10
	v_lshlrev_b32_e32 v9, 1, v9
	v_add_u32_e32 v9, 0xf000, v9
	v_lshlrev_b32_e32 v10, 1, v2
	v_add_u32_e32 v10, 0xf300, v10
	v_cndmask_b32_e64 v168, v10, v9, s[58:59]
	v_cmp_gt_u32_e32 vcc, 136, v0
	v_lshlrev_b32_e32 v9, 2, v0
	v_mov_b32_e32 v10, 0
	s_and_saveexec_b64 s[44:45], vcc
	ds_write_b32 v9, v10 offset:62720
	s_mov_b64 exec, s[44:45]
	v_and_b32_e32 v9, 14, v3
	v_cmp_eq_u32_e64 s[62:63], 2, v9
	v_mov_b32_e32 v10, 0xf500
	s_nop 1
	v_cndmask_b32_e64 v167, v167, v10, s[62:63]
	v_cmp_eq_u32_e64 s[64:65], 0, v9
	v_cmp_eq_u32_e64 s[66:67], 4, v9
	s_or_b64 s[64:65], s[64:65], s[66:67]
	v_cmp_gt_u32_e64 s[66:67], 2, v4
	s_and_b64 s[64:65], s[64:65], s[66:67]
	s_andn2_b64 s[66:67], s[62:63], s[66:67]
	s_or_b64 s[64:65], s[64:65], s[66:67]
	v_and_b32_e32 v9, 1, v4
	v_lshlrev_b32_e32 v9, 5, v9
	v_and_b32_e32 v11, 1, v3
	v_lshl_or_b32 v9, v11, 4, v9
	v_add_u32_e32 v9, 0xf100, v9
	v_cndmask_b32_e64 v96, v10, v9, s[64:65]
	s_mul_i32 s35, s4, 0x25350
	s_add_u32 s14, s14, s35
	s_addc_u32 s15, s15, 0
	s_add_u32 s18, s18, 0x25800
	s_addc_u32 s19, s19, 0
	v_lshlrev_b32_e32 v9, 2, v0
	v_mov_b32_e32 v10, s18
	v_mov_b32_e32 v11, s19
	v_mov_b32_e32 v12, s14
	v_mov_b32_e32 v13, s15
	v_cndmask_b32_e64 v9, v9, v8, s[58:59]
	v_cndmask_b32_e64 v10, v10, v12, s[58:59]
	v_cndmask_b32_e64 v11, v11, v13, s[58:59]
	v_add_co_u32_e32 v170, vcc, v10, v9
	s_nop 1
	v_addc_co_u32_e32 v171, vcc, 0, v11, vcc
	v_mov_b32_e32 v161, 0
	v_mov_b32_e32 v137, 0
	v_mov_b32_e32 v138, 0
	v_mov_b32_e32 v139, 0
	v_mov_b32_e32 v141, 0
	v_mov_b32_e32 v142, 0
	v_mov_b32_e32 v143, 0
	v_mov_b32_e32 v145, 0
	v_mov_b32_e32 v146, 0
	v_mov_b32_e32 v147, 0
	v_mov_b32_e32 v149, 0
	v_mov_b32_e32 v150, 0
	v_mov_b32_e32 v151, 0
	v_mov_b32_e32 v209, 0
	v_mov_b32_e32 v210, 0
	v_mov_b32_e32 v211, 0
	v_mov_b32_e32 v213, 0
	v_mov_b32_e32 v214, 0
	v_mov_b32_e32 v215, 0
	v_mov_b32_e32 v217, 0
	v_mov_b32_e32 v218, 0
	v_mov_b32_e32 v219, 0
	v_mov_b32_e32 v221, 0
	v_mov_b32_e32 v222, 0
	v_mov_b32_e32 v223, 0
	s_mov_b32 s26, 0
	s_waitcnt vmcnt(0) lgkmcnt(0)
	s_barrier
	ds_read_b32 v136, v163 offset:0
	ds_read_b32 v140, v164 offset:0
	ds_read_b32 v148, v165 offset:0
	ds_read_b32 v152, v166 offset:0
	v_mov_b32_e32 v144, v113
	s_waitcnt lgkmcnt(0)

.Lgru2_nostore:
	v_add_f32_e32 v156, v148, v149
	v_add_f32_e32 v159, v136, v137
	v_smfmac_f32_16x16x64_f16 v[144:147], v[120:123], v[56:63], v112
	v_add_f32_e32 v97, v138, v139
	v_add_f32_e32 v98, v150, v151
	v_mov_b32_dpp v159, v156 quad_perm:[0,1,2,3] row_mask:0x2 bank_mask:0xf
	v_exp_f32_e32 v159, v159
	v_smfmac_f32_16x16x64_f16 v[140:143], v[120:123], v[40:47], v112
	v_mov_b32_e32 v210, 0
	v_mov_b32_e32 v211, 0
	v_mov_b32_e32 v222, 0
	v_mov_b32_e32 v223, 0
	v_add_f32_e32 v159, 1.0, v159
	v_rcp_f32_e32 v159, v159
	s_nop 0
	v_add_f32_e32 v155, v144, v145
	v_add_f32_e32 v155, v155, v98
	v_mov_b32_dpp v155, v156 row_shl:6 row_mask:0x2 bank_mask:0xf
	v_fmac_f32_e32 v152, v159, v155
	v_exp_f32_e32 v152, v152
	v_add_f32_e32 v160, v140, v141
	v_add_f32_e32 v160, v160, v97
	v_mov_b32_dpp v160, v156 row_shl:3 row_mask:0x2 bank_mask:0xf
	v_add_f32_e32 v152, 1.0, v152
	v_rcp_f32_e32 v159, v152
	v_exp_f32_e32 v160, v160
	v_fma_f32 v159, v159, -2.0, 1.0
	v_add_f32_e32 v160, 1.0, v160
	v_rcp_f32_e32 v160, v160
	v_sub_f32_e32 v153, v161, v159
	v_fma_f32 v161, v160, v153, v159
	v_fma_mixlo_f16 v162, v160, v153, v159
	ds_write_b16 v168, v162 offset:384
	s_waitcnt lgkmcnt(0)
	s_barrier
	ds_read_b128 v[116:119], v167 offset:384
	ds_read_b128 v[120:123], v167 offset:512
	ds_read_b128 v[124:127], v96 offset:384
	s_waitcnt lgkmcnt(2)
	v_smfmac_f32_16x16x64_f16 v[208:211], v[116:119], v[16:23], v112
	v_smfmac_f32_16x16x64_f16 v[220:223], v[116:119], v[64:71], v112
	s_waitcnt lgkmcnt(1)
	v_smfmac_f32_16x16x64_f16 v[208:211], v[120:123], v[24:31], v112
	v_smfmac_f32_16x16x64_f16 v[220:223], v[120:123], v[72:79], v112
	s_waitcnt lgkmcnt(0)
	v_smfmac_f32_16x16x64_f16 v[208:211], v[124:127], v[80:87], v112
	ds_read_b32 v136, v163 offset:3840
	v_smfmac_f32_16x16x64_f16 v[220:223], v[124:127], v[88:95], v112
	ds_read_b32 v148, v165 offset:3840
	s_cmp_eq_u32 s26, 7
	s_cbranch_scc1 .Lgru2_nopf
	s_add_u32 s22, s22, s27
	s_addc_u32 s23, s23, s50
	s_add_u32 s46, s46, s27
	s_addc_u32 s47, s47, s50
	s_add_u32 s24, s24, s27
	s_addc_u32 s25, s25, s50
	s_add_u32 s48, s48, s27
	s_addc_u32 s49, s49, s50
	global_load_dwordx2 v[176:177], v172, s[22:23] offset:0
	global_load_dwordx2 v[178:179], v172, s[22:23] offset:512
	global_load_dwordx2 v[180:181], v172, s[22:23] offset:1024
	global_load_dwordx2 v[192:193], v172, s[24:25] offset:0
	global_load_dwordx2 v[194:195], v172, s[24:25] offset:512
	global_load_dwordx2 v[196:197], v172, s[24:25] offset:1024
	global_load_dwordx2 v[184:185], v172, s[46:47] offset:0
	global_load_dwordx2 v[186:187], v172, s[46:47] offset:512
	global_load_dwordx2 v[188:189], v172, s[46:47] offset:1024
	global_load_dwordx2 v[200:201], v172, s[48:49] offset:0
	global_load_dwordx2 v[202:203], v172, s[48:49] offset:512
	global_load_dwordx2 v[204:205], v172, s[48:49] offset:1024
	global_load_dwordx2 v[182:183], v114, s[22:23] offset:1536
	global_load_dwordx2 v[198:199], v114, s[24:25] offset:1536
	global_load_dwordx2 v[190:191], v114, s[46:47] offset:1536
	global_load_dwordx2 v[206:207], v114, s[48:49] offset:1536
.Lgru2_nopf:
	v_smfmac_f32_16x16x64_f16 v[216:219], v[116:119], v[48:55], v112
	ds_read_b32 v140, v164 offset:3840
	ds_read_b32 v152, v166 offset:3840
	v_mov_b32_e32 v144, v113
	v_smfmac_f32_16x16x64_f16 v[212:215], v[116:119], v[32:39], v112
	v_mov_b32_e32 v137, 0
	v_mov_b32_e32 v141, 0
	v_mov_b32_e32 v145, 0
	v_mov_b32_e32 v149, 0
	global_store_dword v[170:171], v161, off
	v_lshl_add_u64 v[170:171], v[170:171], 0, s[20:21]
	v_add_f32_e32 v156, v220, v221
	v_add_f32_e32 v159, v208, v209
	v_smfmac_f32_16x16x64_f16 v[216:219], v[120:123], v[56:63], v112
	v_add_f32_e32 v97, v210, v211
	v_add_f32_e32 v98, v222, v223
	v_mov_b32_dpp v159, v156 quad_perm:[0,1,2,3] row_mask:0x2 bank_mask:0xf
	v_exp_f32_e32 v159, v159
	v_smfmac_f32_16x16x64_f16 v[212:215], v[120:123], v[40:47], v112
	v_mov_b32_e32 v138, 0
	v_mov_b32_e32 v139, 0
	v_mov_b32_e32 v150, 0
	v_mov_b32_e32 v151, 0
	v_add_f32_e32 v159, 1.0, v159
	v_rcp_f32_e32 v159, v159
	s_nop 0
	v_add_f32_e32 v155, v216, v217
	v_add_f32_e32 v155, v155, v98
	v_mov_b32_dpp v155, v156 row_shl:6 row_mask:0x2 bank_mask:0xf
	v_fmac_f32_e32 v224, v159, v155
	v_exp_f32_e32 v224, v224
	v_add_f32_e32 v160, v212, v213
	v_add_f32_e32 v160, v160, v97
	v_mov_b32_dpp v160, v156 row_shl:3 row_mask:0x2 bank_mask:0xf
	v_add_f32_e32 v224, 1.0, v224
	v_rcp_f32_e32 v159, v224
	v_exp_f32_e32 v160, v160
	v_fma_f32 v159, v159, -2.0, 1.0
	v_add_f32_e32 v160, 1.0, v160
	v_rcp_f32_e32 v160, v160
	v_sub_f32_e32 v153, v161, v159
	v_fma_f32 v161, v160, v153, v159
	v_fma_mixlo_f16 v162, v160, v153, v159
	ds_write_b16 v168, v162 offset:0
	s_waitcnt lgkmcnt(0)
	s_barrier
	ds_read_b128 v[116:119], v167 offset:0
	ds_read_b128 v[120:123], v167 offset:128
	ds_read_b128 v[124:127], v96 offset:0
	s_waitcnt lgkmcnt(2)
	v_smfmac_f32_16x16x64_f16 v[136:139], v[116:119], v[16:23], v112
	v_smfmac_f32_16x16x64_f16 v[148:151], v[116:119], v[64:71], v112
	s_waitcnt lgkmcnt(1)
	v_smfmac_f32_16x16x64_f16 v[136:139], v[120:123], v[24:31], v112
	v_smfmac_f32_16x16x64_f16 v[148:151], v[120:123], v[72:79], v112
	s_waitcnt lgkmcnt(0)
	v_smfmac_f32_16x16x64_f16 v[136:139], v[124:127], v[80:87], v112
	ds_read_b32 v208, v163 offset:5760
	v_smfmac_f32_16x16x64_f16 v[148:151], v[124:127], v[88:95], v112
	ds_read_b32 v220, v165 offset:5760
	v_smfmac_f32_16x16x64_f16 v[144:147], v[116:119], v[48:55], v112
	ds_read_b32 v212, v164 offset:5760
	ds_read_b32 v224, v166 offset:5760
	v_mov_b32_e32 v216, v113
	v_smfmac_f32_16x16x64_f16 v[140:143], v[116:119], v[32:39], v112
	v_mov_b32_e32 v209, 0
	v_mov_b32_e32 v213, 0
	v_mov_b32_e32 v217, 0
	v_mov_b32_e32 v221, 0
	global_store_dword v[170:171], v161, off
	v_lshl_add_u64 v[170:171], v[170:171], 0, s[20:21]
	v_add_f32_e32 v156, v148, v149
	v_add_f32_e32 v159, v136, v137
	v_smfmac_f32_16x16x64_f16 v[144:147], v[120:123], v[56:63], v112
	v_add_f32_e32 v97, v138, v139
	v_add_f32_e32 v98, v150, v151
	v_mov_b32_dpp v159, v156 quad_perm:[0,1,2,3] row_mask:0x2 bank_mask:0xf
	v_exp_f32_e32 v159, v159
	v_smfmac_f32_16x16x64_f16 v[140:143], v[120:123], v[40:47], v112
	v_mov_b32_e32 v210, 0
	v_mov_b32_e32 v211, 0
	v_mov_b32_e32 v222, 0
	v_mov_b32_e32 v223, 0
	v_add_f32_e32 v159, 1.0, v159
	v_rcp_f32_e32 v159, v159
	s_nop 0
	v_add_f32_e32 v155, v144, v145
	v_add_f32_e32 v155, v155, v98
	v_mov_b32_dpp v155, v156 row_shl:6 row_mask:0x2 bank_mask:0xf
	v_fmac_f32_e32 v152, v159, v155
	v_exp_f32_e32 v152, v152
	v_add_f32_e32 v160, v140, v141
	v_add_f32_e32 v160, v160, v97
	v_mov_b32_dpp v160, v156 row_shl:3 row_mask:0x2 bank_mask:0xf
	v_add_f32_e32 v152, 1.0, v152
	v_rcp_f32_e32 v159, v152
	v_exp_f32_e32 v160, v160
	v_fma_f32 v159, v159, -2.0, 1.0
	v_add_f32_e32 v160, 1.0, v160
	v_rcp_f32_e32 v160, v160
	v_sub_f32_e32 v153, v161, v159
	v_fma_f32 v161, v160, v153, v159
	v_fma_mixlo_f16 v162, v160, v153, v159
	ds_write_b16 v168, v162 offset:384
	s_waitcnt lgkmcnt(0)
	s_barrier
	ds_read_b128 v[116:119], v167 offset:384
	ds_read_b128 v[120:123], v167 offset:512
	ds_read_b128 v[124:127], v96 offset:384
	s_waitcnt lgkmcnt(2)
	v_smfmac_f32_16x16x64_f16 v[208:211], v[116:119], v[16:23], v112
	v_smfmac_f32_16x16x64_f16 v[220:223], v[116:119], v[64:71], v112
	s_waitcnt lgkmcnt(1)
	v_smfmac_f32_16x16x64_f16 v[208:211], v[120:123], v[24:31], v112
	v_smfmac_f32_16x16x64_f16 v[220:223], v[120:123], v[72:79], v112
	s_waitcnt lgkmcnt(0)
	v_smfmac_f32_16x16x64_f16 v[208:211], v[124:127], v[80:87], v112
	ds_read_b32 v136, v163 offset:7680
	v_smfmac_f32_16x16x64_f16 v[220:223], v[124:127], v[88:95], v112
	ds_read_b32 v148, v165 offset:7680
	v_smfmac_f32_16x16x64_f16 v[216:219], v[116:119], v[48:55], v112
	ds_read_b32 v140, v164 offset:7680
	ds_read_b32 v152, v166 offset:7680
	v_mov_b32_e32 v144, v113
	v_smfmac_f32_16x16x64_f16 v[212:215], v[116:119], v[32:39], v112
	v_mov_b32_e32 v137, 0
	v_mov_b32_e32 v141, 0
	v_mov_b32_e32 v145, 0
	v_mov_b32_e32 v149, 0
	global_store_dword v[170:171], v161, off
	v_lshl_add_u64 v[170:171], v[170:171], 0, s[20:21]
	v_add_f32_e32 v156, v220, v221
	v_add_f32_e32 v159, v208, v209
	v_smfmac_f32_16x16x64_f16 v[216:219], v[120:123], v[56:63], v112
	v_add_f32_e32 v97, v210, v211
	v_add_f32_e32 v98, v222, v223
	v_mov_b32_dpp v159, v156 quad_perm:[0,1,2,3] row_mask:0x2 bank_mask:0xf
	v_exp_f32_e32 v159, v159
	v_smfmac_f32_16x16x64_f16 v[212:215], v[120:123], v[40:47], v112
	v_mov_b32_e32 v138, 0
	v_mov_b32_e32 v139, 0
	v_mov_b32_e32 v150, 0
	v_mov_b32_e32 v151, 0
	v_add_f32_e32 v159, 1.0, v159
	v_rcp_f32_e32 v159, v159
	s_nop 0
	v_add_f32_e32 v155, v216, v217
	v_add_f32_e32 v155, v155, v98
	v_mov_b32_dpp v155, v156 row_shl:6 row_mask:0x2 bank_mask:0xf
	v_fmac_f32_e32 v224, v159, v155
	v_exp_f32_e32 v224, v224
	v_add_f32_e32 v160, v212, v213
	v_add_f32_e32 v160, v160, v97
	v_mov_b32_dpp v160, v156 row_shl:3 row_mask:0x2 bank_mask:0xf
	v_add_f32_e32 v224, 1.0, v224
	v_rcp_f32_e32 v159, v224
	v_exp_f32_e32 v160, v160
	v_fma_f32 v159, v159, -2.0, 1.0
	v_add_f32_e32 v160, 1.0, v160
	v_rcp_f32_e32 v160, v160
	v_sub_f32_e32 v153, v161, v159
	v_fma_f32 v161, v160, v153, v159
	v_fma_mixlo_f16 v162, v160, v153, v159
	ds_write_b16 v168, v162 offset:0
	s_waitcnt lgkmcnt(0)
	s_barrier
	ds_read_b128 v[116:119], v167 offset:0
	ds_read_b128 v[120:123], v167 offset:128
	ds_read_b128 v[124:127], v96 offset:0
	s_waitcnt lgkmcnt(2)
	v_smfmac_f32_16x16x64_f16 v[136:139], v[116:119], v[16:23], v112
	v_smfmac_f32_16x16x64_f16 v[148:151], v[116:119], v[64:71], v112
	s_waitcnt lgkmcnt(1)
	v_smfmac_f32_16x16x64_f16 v[136:139], v[120:123], v[24:31], v112
	v_smfmac_f32_16x16x64_f16 v[148:151], v[120:123], v[72:79], v112
	s_waitcnt lgkmcnt(0)
	v_smfmac_f32_16x16x64_f16 v[136:139], v[124:127], v[80:87], v112
	ds_read_b32 v208, v163 offset:9600
	v_smfmac_f32_16x16x64_f16 v[148:151], v[124:127], v[88:95], v112
	ds_read_b32 v220, v165 offset:9600
	v_smfmac_f32_16x16x64_f16 v[144:147], v[116:119], v[48:55], v112
	ds_read_b32 v212, v164 offset:9600
	ds_read_b32 v224, v166 offset:9600
	v_mov_b32_e32 v216, v113
	v_smfmac_f32_16x16x64_f16 v[140:143], v[116:119], v[32:39], v112
	v_mov_b32_e32 v209, 0
	v_mov_b32_e32 v213, 0
	v_mov_b32_e32 v217, 0
	v_mov_b32_e32 v221, 0
	global_store_dword v[170:171], v161, off
	v_lshl_add_u64 v[170:171], v[170:171], 0, s[20:21]
	v_add_f32_e32 v156, v148, v149
	v_add_f32_e32 v159, v136, v137
	v_smfmac_f32_16x16x64_f16 v[144:147], v[120:123], v[56:63], v112
	v_add_f32_e32 v97, v138, v139
	v_add_f32_e32 v98, v150, v151
	v_mov_b32_dpp v159, v156 quad_perm:[0,1,2,3] row_mask:0x2 bank_mask:0xf
	v_exp_f32_e32 v159, v159
	v_smfmac_f32_16x16x64_f16 v[140:143], v[120:123], v[40:47], v112
	v_mov_b32_e32 v210, 0
	v_mov_b32_e32 v211, 0
	v_mov_b32_e32 v222, 0
	v_mov_b32_e32 v223, 0
	v_add_f32_e32 v159, 1.0, v159
	v_rcp_f32_e32 v159, v159
	s_nop 0
	v_add_f32_e32 v155, v144, v145
	v_add_f32_e32 v155, v155, v98
	v_mov_b32_dpp v155, v156 row_shl:6 row_mask:0x2 bank_mask:0xf
	v_fmac_f32_e32 v152, v159, v155
	v_exp_f32_e32 v152, v152
	v_add_f32_e32 v160, v140, v141
	v_add_f32_e32 v160, v160, v97
	v_mov_b32_dpp v160, v156 row_shl:3 row_mask:0x2 bank_mask:0xf
	v_add_f32_e32 v152, 1.0, v152
	v_rcp_f32_e32 v159, v152
	v_exp_f32_e32 v160, v160
	v_fma_f32 v159, v159, -2.0, 1.0
	v_add_f32_e32 v160, 1.0, v160
	v_rcp_f32_e32 v160, v160
	v_sub_f32_e32 v153, v161, v159
	v_fma_f32 v161, v160, v153, v159
	v_fma_mixlo_f16 v162, v160, v153, v159
	ds_write_b16 v168, v162 offset:384
	s_waitcnt lgkmcnt(0)
	s_barrier
	ds_read_b128 v[116:119], v167 offset:384
	ds_read_b128 v[120:123], v167 offset:512
	ds_read_b128 v[124:127], v96 offset:384
	s_waitcnt lgkmcnt(2)
	v_smfmac_f32_16x16x64_f16 v[208:211], v[116:119], v[16:23], v112
	v_smfmac_f32_16x16x64_f16 v[220:223], v[116:119], v[64:71], v112
	s_waitcnt lgkmcnt(1)
	v_smfmac_f32_16x16x64_f16 v[208:211], v[120:123], v[24:31], v112
	v_smfmac_f32_16x16x64_f16 v[220:223], v[120:123], v[72:79], v112
	s_waitcnt lgkmcnt(0)
	v_smfmac_f32_16x16x64_f16 v[208:211], v[124:127], v[80:87], v112
	ds_read_b32 v136, v163 offset:11520
	v_smfmac_f32_16x16x64_f16 v[220:223], v[124:127], v[88:95], v112
	ds_read_b32 v148, v165 offset:11520
	v_smfmac_f32_16x16x64_f16 v[216:219], v[116:119], v[48:55], v112
	ds_read_b32 v140, v164 offset:11520
	ds_read_b32 v152, v166 offset:11520
	v_mov_b32_e32 v144, v113
	v_smfmac_f32_16x16x64_f16 v[212:215], v[116:119], v[32:39], v112
	v_mov_b32_e32 v137, 0
	v_mov_b32_e32 v141, 0
	v_mov_b32_e32 v145, 0
	v_mov_b32_e32 v149, 0
	global_store_dword v[170:171], v161, off
	v_lshl_add_u64 v[170:171], v[170:171], 0, s[20:21]
	v_add_f32_e32 v156, v220, v221
	v_add_f32_e32 v159, v208, v209
	v_smfmac_f32_16x16x64_f16 v[216:219], v[120:123], v[56:63], v112
	v_add_f32_e32 v97, v210, v211
	v_add_f32_e32 v98, v222, v223
	v_mov_b32_dpp v159, v156 quad_perm:[0,1,2,3] row_mask:0x2 bank_mask:0xf
	v_exp_f32_e32 v159, v159
	v_smfmac_f32_16x16x64_f16 v[212:215], v[120:123], v[40:47], v112
	v_mov_b32_e32 v138, 0
	v_mov_b32_e32 v139, 0
	v_mov_b32_e32 v150, 0
	v_mov_b32_e32 v151, 0
	v_add_f32_e32 v159, 1.0, v159
	v_rcp_f32_e32 v159, v159
	s_nop 0
	v_add_f32_e32 v155, v216, v217
	v_add_f32_e32 v155, v155, v98
	v_mov_b32_dpp v155, v156 row_shl:6 row_mask:0x2 bank_mask:0xf
	v_fmac_f32_e32 v224, v159, v155
	v_exp_f32_e32 v224, v224
	v_add_f32_e32 v160, v212, v213
	v_add_f32_e32 v160, v160, v97
	v_mov_b32_dpp v160, v156 row_shl:3 row_mask:0x2 bank_mask:0xf
	v_add_f32_e32 v224, 1.0, v224
	v_rcp_f32_e32 v159, v224
	v_exp_f32_e32 v160, v160
	v_fma_f32 v159, v159, -2.0, 1.0
	v_add_f32_e32 v160, 1.0, v160
	v_rcp_f32_e32 v160, v160
	v_sub_f32_e32 v153, v161, v159
	v_fma_f32 v161, v160, v153, v159
	v_fma_mixlo_f16 v162, v160, v153, v159
	ds_write_b16 v168, v162 offset:0
	s_waitcnt lgkmcnt(0)
	s_barrier
	ds_read_b128 v[116:119], v167 offset:0
	ds_read_b128 v[120:123], v167 offset:128
	ds_read_b128 v[124:127], v96 offset:0
	s_waitcnt lgkmcnt(2)
	v_smfmac_f32_16x16x64_f16 v[136:139], v[116:119], v[16:23], v112
	v_smfmac_f32_16x16x64_f16 v[148:151], v[116:119], v[64:71], v112
	s_waitcnt lgkmcnt(1)
	v_smfmac_f32_16x16x64_f16 v[136:139], v[120:123], v[24:31], v112
	v_smfmac_f32_16x16x64_f16 v[148:151], v[120:123], v[72:79], v112
	s_waitcnt lgkmcnt(0)
	v_smfmac_f32_16x16x64_f16 v[136:139], v[124:127], v[80:87], v112
	ds_read_b32 v208, v163 offset:13440
	v_smfmac_f32_16x16x64_f16 v[148:151], v[124:127], v[88:95], v112
	ds_read_b32 v220, v165 offset:13440
	v_smfmac_f32_16x16x64_f16 v[144:147], v[116:119], v[48:55], v112
	ds_read_b32 v212, v164 offset:13440
	ds_read_b32 v224, v166 offset:13440
	v_mov_b32_e32 v216, v113
	v_smfmac_f32_16x16x64_f16 v[140:143], v[116:119], v[32:39], v112
	v_mov_b32_e32 v209, 0
	v_mov_b32_e32 v213, 0
	v_mov_b32_e32 v217, 0
	v_mov_b32_e32 v221, 0
	global_store_dword v[170:171], v161, off
	v_lshl_add_u64 v[170:171], v[170:171], 0, s[20:21]
	v_add_f32_e32 v156, v148, v149
	v_add_f32_e32 v159, v136, v137
	v_smfmac_f32_16x16x64_f16 v[144:147], v[120:123], v[56:63], v112
	v_add_f32_e32 v97, v138, v139
	v_add_f32_e32 v98, v150, v151
	v_mov_b32_dpp v159, v156 quad_perm:[0,1,2,3] row_mask:0x2 bank_mask:0xf
	v_exp_f32_e32 v159, v159
	v_smfmac_f32_16x16x64_f16 v[140:143], v[120:123], v[40:47], v112
	v_mov_b32_e32 v210, 0
	v_mov_b32_e32 v211, 0
	v_mov_b32_e32 v222, 0
	v_mov_b32_e32 v223, 0
	v_add_f32_e32 v159, 1.0, v159
	v_rcp_f32_e32 v159, v159
	s_nop 0
	v_add_f32_e32 v155, v144, v145
	v_add_f32_e32 v155, v155, v98
	v_mov_b32_dpp v155, v156 row_shl:6 row_mask:0x2 bank_mask:0xf
	v_fmac_f32_e32 v152, v159, v155
	v_exp_f32_e32 v152, v152
	v_add_f32_e32 v160, v140, v141
	v_add_f32_e32 v160, v160, v97
	v_mov_b32_dpp v160, v156 row_shl:3 row_mask:0x2 bank_mask:0xf
	v_add_f32_e32 v152, 1.0, v152
	v_rcp_f32_e32 v159, v152
	v_exp_f32_e32 v160, v160
	v_fma_f32 v159, v159, -2.0, 1.0
	v_add_f32_e32 v160, 1.0, v160
	v_rcp_f32_e32 v160, v160
	v_sub_f32_e32 v153, v161, v159
	v_fma_f32 v161, v160, v153, v159
	v_fma_mixlo_f16 v162, v160, v153, v159
	ds_write_b16 v168, v162 offset:384
	s_waitcnt lgkmcnt(0)
	s_barrier
	ds_read_b128 v[116:119], v167 offset:384
	ds_read_b128 v[120:123], v167 offset:512
	ds_read_b128 v[124:127], v96 offset:384
	s_waitcnt lgkmcnt(2)
	v_smfmac_f32_16x16x64_f16 v[208:211], v[116:119], v[16:23], v112
	v_smfmac_f32_16x16x64_f16 v[220:223], v[116:119], v[64:71], v112
	s_waitcnt lgkmcnt(1)
	v_smfmac_f32_16x16x64_f16 v[208:211], v[120:123], v[24:31], v112
	v_smfmac_f32_16x16x64_f16 v[220:223], v[120:123], v[72:79], v112
	s_waitcnt lgkmcnt(0)
	v_smfmac_f32_16x16x64_f16 v[208:211], v[124:127], v[80:87], v112
	ds_read_b32 v136, v163 offset:15360
	v_smfmac_f32_16x16x64_f16 v[220:223], v[124:127], v[88:95], v112
	ds_read_b32 v148, v165 offset:15360
	v_smfmac_f32_16x16x64_f16 v[216:219], v[116:119], v[48:55], v112
	ds_read_b32 v140, v164 offset:15360
	ds_read_b32 v152, v166 offset:15360
	v_mov_b32_e32 v144, v113
	v_smfmac_f32_16x16x64_f16 v[212:215], v[116:119], v[32:39], v112
	v_mov_b32_e32 v137, 0
	v_mov_b32_e32 v141, 0
	v_mov_b32_e32 v145, 0
	v_mov_b32_e32 v149, 0
	global_store_dword v[170:171], v161, off
	v_lshl_add_u64 v[170:171], v[170:171], 0, s[20:21]
	v_add_f32_e32 v156, v220, v221
	v_add_f32_e32 v159, v208, v209
	v_smfmac_f32_16x16x64_f16 v[216:219], v[120:123], v[56:63], v112
	v_add_f32_e32 v97, v210, v211
	v_add_f32_e32 v98, v222, v223
	v_mov_b32_dpp v159, v156 quad_perm:[0,1,2,3] row_mask:0x2 bank_mask:0xf
	v_exp_f32_e32 v159, v159
	v_smfmac_f32_16x16x64_f16 v[212:215], v[120:123], v[40:47], v112
	v_mov_b32_e32 v138, 0
	v_mov_b32_e32 v139, 0
	v_mov_b32_e32 v150, 0
	v_mov_b32_e32 v151, 0
	v_add_f32_e32 v159, 1.0, v159
	v_rcp_f32_e32 v159, v159
	s_nop 0
	v_add_f32_e32 v155, v216, v217
	v_add_f32_e32 v155, v155, v98
	v_mov_b32_dpp v155, v156 row_shl:6 row_mask:0x2 bank_mask:0xf
	v_fmac_f32_e32 v224, v159, v155
	v_exp_f32_e32 v224, v224
	v_add_f32_e32 v160, v212, v213
	v_add_f32_e32 v160, v160, v97
	v_mov_b32_dpp v160, v156 row_shl:3 row_mask:0x2 bank_mask:0xf
	v_add_f32_e32 v224, 1.0, v224
	v_rcp_f32_e32 v159, v224
	v_exp_f32_e32 v160, v160
	v_fma_f32 v159, v159, -2.0, 1.0
	v_add_f32_e32 v160, 1.0, v160
	v_rcp_f32_e32 v160, v160
	v_sub_f32_e32 v153, v161, v159
	v_fma_f32 v161, v160, v153, v159
	v_fma_mixlo_f16 v162, v160, v153, v159
	ds_write_b16 v168, v162 offset:0
	s_waitcnt lgkmcnt(0)
	s_barrier
	ds_read_b128 v[116:119], v167 offset:0
	ds_read_b128 v[120:123], v167 offset:128
	ds_read_b128 v[124:127], v96 offset:0
	s_waitcnt lgkmcnt(2)
	v_smfmac_f32_16x16x64_f16 v[136:139], v[116:119], v[16:23], v112
	v_smfmac_f32_16x16x64_f16 v[148:151], v[116:119], v[64:71], v112
	s_waitcnt lgkmcnt(1)
	v_smfmac_f32_16x16x64_f16 v[136:139], v[120:123], v[24:31], v112
	v_smfmac_f32_16x16x64_f16 v[148:151], v[120:123], v[72:79], v112
	s_waitcnt lgkmcnt(0)
	v_smfmac_f32_16x16x64_f16 v[136:139], v[124:127], v[80:87], v112
	ds_read_b32 v208, v163 offset:17280
	v_smfmac_f32_16x16x64_f16 v[148:151], v[124:127], v[88:95], v112
	ds_read_b32 v220, v165 offset:17280
	v_smfmac_f32_16x16x64_f16 v[144:147], v[116:119], v[48:55], v112
	ds_read_b32 v212, v164 offset:17280
	ds_read_b32 v224, v166 offset:17280
	v_mov_b32_e32 v216, v113
	v_smfmac_f32_16x16x64_f16 v[140:143], v[116:119], v[32:39], v112
	v_mov_b32_e32 v209, 0
	v_mov_b32_e32 v213, 0
	v_mov_b32_e32 v217, 0
	v_mov_b32_e32 v221, 0
	global_store_dword v[170:171], v161, off
	v_lshl_add_u64 v[170:171], v[170:171], 0, s[20:21]
	v_add_f32_e32 v156, v148, v149
	v_add_f32_e32 v159, v136, v137
	v_smfmac_f32_16x16x64_f16 v[144:147], v[120:123], v[56:63], v112
	v_add_f32_e32 v97, v138, v139
	v_add_f32_e32 v98, v150, v151
	v_mov_b32_dpp v159, v156 quad_perm:[0,1,2,3] row_mask:0x2 bank_mask:0xf
	v_exp_f32_e32 v159, v159
	v_smfmac_f32_16x16x64_f16 v[140:143], v[120:123], v[40:47], v112
	v_mov_b32_e32 v210, 0
	v_mov_b32_e32 v211, 0
	v_mov_b32_e32 v222, 0
	v_mov_b32_e32 v223, 0
	v_add_f32_e32 v159, 1.0, v159
	v_rcp_f32_e32 v159, v159
	s_nop 0
	v_add_f32_e32 v155, v144, v145
	v_add_f32_e32 v155, v155, v98
	v_mov_b32_dpp v155, v156 row_shl:6 row_mask:0x2 bank_mask:0xf
	v_fmac_f32_e32 v152, v159, v155
	v_exp_f32_e32 v152, v152
	v_add_f32_e32 v160, v140, v141
	v_add_f32_e32 v160, v160, v97
	v_mov_b32_dpp v160, v156 row_shl:3 row_mask:0x2 bank_mask:0xf
	v_add_f32_e32 v152, 1.0, v152
	v_rcp_f32_e32 v159, v152
	v_exp_f32_e32 v160, v160
	v_fma_f32 v159, v159, -2.0, 1.0
	v_add_f32_e32 v160, 1.0, v160
	v_rcp_f32_e32 v160, v160
	v_sub_f32_e32 v153, v161, v159
	v_fma_f32 v161, v160, v153, v159
	v_fma_mixlo_f16 v162, v160, v153, v159
	ds_write_b16 v168, v162 offset:384
	s_waitcnt lgkmcnt(0)
	s_barrier
	ds_read_b128 v[116:119], v167 offset:384
	ds_read_b128 v[120:123], v167 offset:512
	ds_read_b128 v[124:127], v96 offset:384
	s_waitcnt lgkmcnt(2)
	v_smfmac_f32_16x16x64_f16 v[208:211], v[116:119], v[16:23], v112
	v_smfmac_f32_16x16x64_f16 v[220:223], v[116:119], v[64:71], v112
	s_waitcnt lgkmcnt(1)
	v_smfmac_f32_16x16x64_f16 v[208:211], v[120:123], v[24:31], v112
	v_smfmac_f32_16x16x64_f16 v[220:223], v[120:123], v[72:79], v112
	s_waitcnt lgkmcnt(0)
	v_smfmac_f32_16x16x64_f16 v[208:211], v[124:127], v[80:87], v112
	ds_read_b32 v136, v163 offset:19200
	v_smfmac_f32_16x16x64_f16 v[220:223], v[124:127], v[88:95], v112
	ds_read_b32 v148, v165 offset:19200
	s_cmp_eq_u32 s26, 7
	s_cbranch_scc1 .Lgru2_nost0
	s_waitcnt vmcnt(4)
	v_add_f32_e32 v176, v176, v192
	v_add_f32_e32 v177, v177, v193
	v_mul_f32_e32 v176, s51, v176
	v_mul_f32_e32 v177, s51, v177
	v_add_f32_e32 v178, v178, v194
	v_add_f32_e32 v179, v179, v195
	v_mul_f32_e32 v178, s51, v178
	v_mul_f32_e32 v179, s51, v179
	v_add_f32_e32 v180, v180, v196
	v_add_f32_e32 v181, v181, v197
	v_mul_f32_e32 v180, v175, v180
	v_mul_f32_e32 v181, v175, v181
	v_add_f32_e32 v182, v182, v198
	v_add_f32_e32 v183, v183, v199
	v_mul_f32_e32 v182, s52, v182
	v_mul_f32_e32 v183, s52, v183
	ds_write_b64 v173, v[176:177] offset:0
	ds_write_b64 v173, v[178:179] offset:512
	ds_write_b64 v173, v[180:181] offset:1024
	ds_write_b64 v115, v[182:183] offset:1536
.Lgru2_nost0:
	v_smfmac_f32_16x16x64_f16 v[216:219], v[116:119], v[48:55], v112
	ds_read_b32 v140, v164 offset:19200
	ds_read_b32 v152, v166 offset:19200
	v_mov_b32_e32 v144, v113
	v_smfmac_f32_16x16x64_f16 v[212:215], v[116:119], v[32:39], v112
	v_mov_b32_e32 v137, 0
	v_mov_b32_e32 v141, 0
	v_mov_b32_e32 v145, 0
	v_mov_b32_e32 v149, 0
	global_store_dword v[170:171], v161, off
	v_lshl_add_u64 v[170:171], v[170:171], 0, s[20:21]
	v_add_f32_e32 v156, v220, v221
	v_add_f32_e32 v159, v208, v209
	v_smfmac_f32_16x16x64_f16 v[216:219], v[120:123], v[56:63], v112
	v_add_f32_e32 v97, v210, v211
	v_add_f32_e32 v98, v222, v223
	v_mov_b32_dpp v159, v156 quad_perm:[0,1,2,3] row_mask:0x2 bank_mask:0xf
	v_exp_f32_e32 v159, v159
	v_smfmac_f32_16x16x64_f16 v[212:215], v[120:123], v[40:47], v112
	v_mov_b32_e32 v138, 0
	v_mov_b32_e32 v139, 0
	v_mov_b32_e32 v150, 0
	v_mov_b32_e32 v151, 0
	v_add_f32_e32 v159, 1.0, v159
	v_rcp_f32_e32 v159, v159
	s_nop 0
	v_add_f32_e32 v155, v216, v217
	v_add_f32_e32 v155, v155, v98
	v_mov_b32_dpp v155, v156 row_shl:6 row_mask:0x2 bank_mask:0xf
	v_fmac_f32_e32 v224, v159, v155
	v_exp_f32_e32 v224, v224
	v_add_f32_e32 v160, v212, v213
	v_add_f32_e32 v160, v160, v97
	v_mov_b32_dpp v160, v156 row_shl:3 row_mask:0x2 bank_mask:0xf
	v_add_f32_e32 v224, 1.0, v224
	v_rcp_f32_e32 v159, v224
	v_exp_f32_e32 v160, v160
	v_fma_f32 v159, v159, -2.0, 1.0
	v_add_f32_e32 v160, 1.0, v160
	v_rcp_f32_e32 v160, v160
	v_sub_f32_e32 v153, v161, v159
	v_fma_f32 v161, v160, v153, v159
	v_fma_mixlo_f16 v162, v160, v153, v159
	ds_write_b16 v168, v162 offset:0
	s_waitcnt lgkmcnt(0)
	s_barrier
	ds_read_b128 v[116:119], v167 offset:0
	ds_read_b128 v[120:123], v167 offset:128
	ds_read_b128 v[124:127], v96 offset:0
	s_waitcnt lgkmcnt(2)
	v_smfmac_f32_16x16x64_f16 v[136:139], v[116:119], v[16:23], v112
	v_smfmac_f32_16x16x64_f16 v[148:151], v[116:119], v[64:71], v112
	s_waitcnt lgkmcnt(1)
	v_smfmac_f32_16x16x64_f16 v[136:139], v[120:123], v[24:31], v112
	v_smfmac_f32_16x16x64_f16 v[148:151], v[120:123], v[72:79], v112
	s_waitcnt lgkmcnt(0)
	v_smfmac_f32_16x16x64_f16 v[136:139], v[124:127], v[80:87], v112
	ds_read_b32 v208, v163 offset:21120
	v_smfmac_f32_16x16x64_f16 v[148:151], v[124:127], v[88:95], v112
	ds_read_b32 v220, v165 offset:21120
	v_smfmac_f32_16x16x64_f16 v[144:147], v[116:119], v[48:55], v112
	ds_read_b32 v212, v164 offset:21120
	ds_read_b32 v224, v166 offset:21120
	v_mov_b32_e32 v216, v113
	v_smfmac_f32_16x16x64_f16 v[140:143], v[116:119], v[32:39], v112
	v_mov_b32_e32 v209, 0
	v_mov_b32_e32 v213, 0
	v_mov_b32_e32 v217, 0
	v_mov_b32_e32 v221, 0
	global_store_dword v[170:171], v161, off
	v_lshl_add_u64 v[170:171], v[170:171], 0, s[20:21]
	v_add_f32_e32 v156, v148, v149
	v_add_f32_e32 v159, v136, v137
	v_smfmac_f32_16x16x64_f16 v[144:147], v[120:123], v[56:63], v112
	v_add_f32_e32 v97, v138, v139
	v_add_f32_e32 v98, v150, v151
	v_mov_b32_dpp v159, v156 quad_perm:[0,1,2,3] row_mask:0x2 bank_mask:0xf
	v_exp_f32_e32 v159, v159
	v_smfmac_f32_16x16x64_f16 v[140:143], v[120:123], v[40:47], v112
	v_mov_b32_e32 v210, 0
	v_mov_b32_e32 v211, 0
	v_mov_b32_e32 v222, 0
	v_mov_b32_e32 v223, 0
	v_add_f32_e32 v159, 1.0, v159
	v_rcp_f32_e32 v159, v159
	s_nop 0
	v_add_f32_e32 v155, v144, v145
	v_add_f32_e32 v155, v155, v98
	v_mov_b32_dpp v155, v156 row_shl:6 row_mask:0x2 bank_mask:0xf
	v_fmac_f32_e32 v152, v159, v155
	v_exp_f32_e32 v152, v152
	v_add_f32_e32 v160, v140, v141
	v_add_f32_e32 v160, v160, v97
	v_mov_b32_dpp v160, v156 row_shl:3 row_mask:0x2 bank_mask:0xf
	v_add_f32_e32 v152, 1.0, v152
	v_rcp_f32_e32 v159, v152
	v_exp_f32_e32 v160, v160
	v_fma_f32 v159, v159, -2.0, 1.0
	v_add_f32_e32 v160, 1.0, v160
	v_rcp_f32_e32 v160, v160
	v_sub_f32_e32 v153, v161, v159
	v_fma_f32 v161, v160, v153, v159
	v_fma_mixlo_f16 v162, v160, v153, v159
	ds_write_b16 v168, v162 offset:384
	s_waitcnt lgkmcnt(0)
	s_barrier
	ds_read_b128 v[116:119], v167 offset:384
	ds_read_b128 v[120:123], v167 offset:512
	ds_read_b128 v[124:127], v96 offset:384
	s_waitcnt lgkmcnt(2)
	v_smfmac_f32_16x16x64_f16 v[208:211], v[116:119], v[16:23], v112
	v_smfmac_f32_16x16x64_f16 v[220:223], v[116:119], v[64:71], v112
	s_waitcnt lgkmcnt(1)
	v_smfmac_f32_16x16x64_f16 v[208:211], v[120:123], v[24:31], v112
	v_smfmac_f32_16x16x64_f16 v[220:223], v[120:123], v[72:79], v112
	s_waitcnt lgkmcnt(0)
	v_smfmac_f32_16x16x64_f16 v[208:211], v[124:127], v[80:87], v112
	ds_read_b32 v136, v163 offset:23040
	v_smfmac_f32_16x16x64_f16 v[220:223], v[124:127], v[88:95], v112
	ds_read_b32 v148, v165 offset:23040
	s_cmp_eq_u32 s26, 7
	s_cbranch_scc1 .Lgru2_nost1
	s_waitcnt vmcnt(4)
	v_add_f32_e32 v184, v184, v200
	v_add_f32_e32 v185, v185, v201
	v_mul_f32_e32 v184, s51, v184
	v_mul_f32_e32 v185, s51, v185
	v_add_f32_e32 v186, v186, v202
	v_add_f32_e32 v187, v187, v203
	v_mul_f32_e32 v186, s51, v186
	v_mul_f32_e32 v187, s51, v187
	v_add_f32_e32 v188, v188, v204
	v_add_f32_e32 v189, v189, v205
	v_mul_f32_e32 v188, v175, v188
	v_mul_f32_e32 v189, v175, v189
	v_add_f32_e32 v190, v190, v206
	v_add_f32_e32 v191, v191, v207
	v_mul_f32_e32 v190, s52, v190
	v_mul_f32_e32 v191, s52, v191
	ds_write_b64 v174, v[184:185] offset:0
	ds_write_b64 v174, v[186:187] offset:512
	ds_write_b64 v174, v[188:189] offset:1024
	ds_write_b64 v169, v[190:191] offset:1536

	.amdhsa_kernel _Z15gru_mfma_kernelILi2EEvPKfmS1_S1_S1_S1_PfS2_i7PreArgs
		.amdhsa_group_segment_fixed_size 64480
		.amdhsa_private_segment_fixed_size 0
		.amdhsa_kernarg_size 448
		.amdhsa_user_sgpr_count 2
		.amdhsa_user_sgpr_dispatch_ptr 0
		.amdhsa_user_sgpr_queue_ptr 0
		.amdhsa_user_sgpr_kernarg_segment_ptr 1
		.amdhsa_user_sgpr_dispatch_id 0
		.amdhsa_user_sgpr_kernarg_preload_length 0
		.amdhsa_user_sgpr_kernarg_preload_offset 0
		.amdhsa_user_sgpr_private_segment_size 0
		.amdhsa_uses_dynamic_stack 0
		.amdhsa_enable_private_segment 0
		.amdhsa_system_sgpr_workgroup_id_x 1
		.amdhsa_system_sgpr_workgroup_id_y 0
		.amdhsa_system_sgpr_workgroup_id_z 0
		.amdhsa_system_sgpr_workgroup_info 0
		.amdhsa_system_vgpr_workitem_id 0
		.amdhsa_next_free_vgpr 232
		.amdhsa_next_free_sgpr 96
		.amdhsa_accum_offset 232
		.amdhsa_reserve_vcc 1
		.amdhsa_float_round_mode_32 0
		.amdhsa_float_round_mode_16_64 0
		.amdhsa_float_denorm_mode_32 3
		.amdhsa_float_denorm_mode_16_64 3
		.amdhsa_dx10_clamp 1
		.amdhsa_ieee_mode 1
		.amdhsa_fp16_overflow 0
		.amdhsa_tg_split 0
		.amdhsa_exception_fp_ieee_invalid_op 0
		.amdhsa_exception_fp_denorm_src 0
		.amdhsa_exception_fp_ieee_div_zero 0
		.amdhsa_exception_fp_ieee_overflow 0
		.amdhsa_exception_fp_ieee_underflow 0
		.amdhsa_exception_fp_ieee_inexact 0
		.amdhsa_exception_int_div_zero 0
	.end_amdhsa_kernel

amdhsa.kernels:
  - .agpr_count:     16
    .args:
      - .actual_access:  read_only
        .address_space:  global
        .offset:         0
        .size:           8
        .value_kind:     global_buffer
      - .actual_access:  read_only
        .address_space:  global
        .offset:         8
        .size:           8
        .value_kind:     global_buffer
      - .actual_access:  read_only
        .address_space:  global
        .offset:         16
        .size:           8
        .value_kind:     global_buffer
      - .actual_access:  read_only
        .address_space:  global
        .offset:         24
        .size:           8
        .value_kind:     global_buffer
      - .actual_access:  write_only
        .address_space:  global
        .offset:         32
        .size:           8
        .value_kind:     global_buffer
      - .offset:         40
        .size:           4
        .value_kind:     by_value
      - .offset:         44
        .size:           4
        .value_kind:     by_value
      - .offset:         48
        .size:           4
        .value_kind:     by_value
      - .offset:         52
        .size:           4
        .value_kind:     by_value
      - .offset:         56
        .size:           4
        .value_kind:     by_value
      - .offset:         60
        .size:           4
        .value_kind:     by_value
      - .offset:         64
        .size:           4
        .value_kind:     by_value
    .group_segment_fixed_size: 43008
    .kernarg_segment_align: 8
    .kernarg_segment_size: 68
    .language:       OpenCL C
    .language_version:
      - 2
      - 0
    .max_flat_workgroup_size: 256
    .name:           _Z15gemm_f16_kernelPKDF16_S0_PKfS2_Pfiiiiiii
    .private_segment_fixed_size: 0
    .sgpr_count:     33
    .sgpr_spill_count: 0
    .symbol:         _Z15gemm_f16_kernelPKDF16_S0_PKfS2_Pfiiiiiii.kd
    .uniform_work_group_size: 1
    .uses_dynamic_stack: false
    .vgpr_count:     104
    .vgpr_spill_count: 0
    .wavefront_size: 64
  - .agpr_count:     0
    .args:
      - .actual_access:  read_only
        .address_space:  global
        .offset:         0
        .size:           8
        .value_kind:     global_buffer
      - .actual_access:  read_only
        .address_space:  global
        .offset:         8
        .size:           8
        .value_kind:     global_buffer
      - .actual_access:  read_only
        .address_space:  global
        .offset:         16
        .size:           8
        .value_kind:     global_buffer
      - .actual_access:  read_only
        .address_space:  global
        .offset:         24
        .size:           8
        .value_kind:     global_buffer
      - .actual_access:  read_only
        .address_space:  global
        .offset:         32
        .size:           8
        .value_kind:     global_buffer
      - .actual_access:  read_only
        .address_space:  global
        .offset:         40
        .size:           8
        .value_kind:     global_buffer
      - .actual_access:  write_only
        .address_space:  global
        .offset:         48
        .size:           8
        .value_kind:     global_buffer
      - .actual_access:  read_only
        .address_space:  global
        .offset:         56
        .size:           8
        .value_kind:     global_buffer
    .group_segment_fixed_size: 121472
    .kernarg_segment_align: 8
    .kernarg_segment_size: 64
    .language:       OpenCL C
    .language_version:
      - 2
      - 0
    .max_flat_workgroup_size: 512
    .name:           _Z15score_ds_kernelPKfS0_S0_S0_S0_S0_PfPKDF16_
    .private_segment_fixed_size: 0
    .sgpr_count:     32
    .sgpr_spill_count: 0
    .symbol:         _Z15score_ds_kernelPKfS0_S0_S0_S0_S0_PfPKDF16_.kd
    .uniform_work_group_size: 1
    .uses_dynamic_stack: false
    .vgpr_count:     254
    .vgpr_spill_count: 0
    .wavefront_size: 64
  - .agpr_count:     0
    .args:
      - .actual_access:  read_only
        .address_space:  global
        .offset:         0
        .size:           8
        .value_kind:     global_buffer
      - .actual_access:  read_only
        .address_space:  global
        .offset:         8
        .size:           8
        .value_kind:     global_buffer
      - .actual_access:  read_only
        .address_space:  global
        .offset:         16
        .size:           8
        .value_kind:     global_buffer
      - .actual_access:  read_only
        .address_space:  global
        .offset:         24
        .size:           8
        .value_kind:     global_buffer
      - .actual_access:  read_only
        .address_space:  global
        .offset:         32
        .size:           8
        .value_kind:     global_buffer
      - .actual_access:  read_only
        .address_space:  global
        .offset:         40
        .size:           8
        .value_kind:     global_buffer
      - .actual_access:  read_only
        .address_space:  global
        .offset:         48
        .size:           8
        .value_kind:     global_buffer
      - .actual_access:  read_only
        .address_space:  global
        .offset:         56
        .size:           8
        .value_kind:     global_buffer
      - .actual_access:  read_only
        .address_space:  global
        .offset:         64
        .size:           8
        .value_kind:     global_buffer
      - .actual_access:  read_only
        .address_space:  global
        .offset:         72
        .size:           8
        .value_kind:     global_buffer
      - .actual_access:  write_only
        .address_space:  global
        .offset:         80
        .size:           8
        .value_kind:     global_buffer
    .group_segment_fixed_size: 70336
    .kernarg_segment_align: 8
    .kernarg_segment_size: 88
    .language:       OpenCL C
    .language_version:
      - 2
      - 0
    .max_flat_workgroup_size: 1024
    .name:           _Z13attend_kernelPKfS0_S0_S0_S0_S0_S0_S0_S0_S0_PDF16_
    .private_segment_fixed_size: 0
    .sgpr_count:     40
    .sgpr_spill_count: 0
    .symbol:         _Z13attend_kernelPKfS0_S0_S0_S0_S0_S0_S0_S0_S0_PDF16_.kd
    .uniform_work_group_size: 1
    .uses_dynamic_stack: false
    .vgpr_count:     86
    .vgpr_spill_count: 0
    .wavefront_size: 64
  - .agpr_count:     0
    .args:
      - .actual_access:  read_only
        .address_space:  global
        .offset:         0
        .size:           8
        .value_kind:     global_buffer
      - .actual_access:  read_only
        .address_space:  global
        .offset:         8
        .size:           8
        .value_kind:     global_buffer
      - .actual_access:  read_only
        .address_space:  global
        .offset:         16
        .size:           8
        .value_kind:     global_buffer
      - .actual_access:  read_only
        .address_space:  global
        .offset:         24
        .size:           8
        .value_kind:     global_buffer
      - .actual_access:  write_only
        .address_space:  global
        .offset:         32
        .size:           8
        .value_kind:     global_buffer
    .group_segment_fixed_size: 9088
    .kernarg_segment_align: 8
    .kernarg_segment_size: 40
    .language:       OpenCL C
    .language_version:
      - 2
      - 0
    .max_flat_workgroup_size: 512
    .name:           _Z16postfinal_kernelPKfS0_S0_S0_Pf
    .private_segment_fixed_size: 0
    .sgpr_count:     30
    .sgpr_spill_count: 0
    .symbol:         _Z16postfinal_kernelPKfS0_S0_S0_Pf.kd
    .uniform_work_group_size: 1
    .uses_dynamic_stack: false
    .vgpr_count:     124
    .vgpr_spill_count: 0
    .wavefront_size: 64
  - .agpr_count:     16
    .args:
      - .offset:         0
        .size:           1136
        .value_kind:     by_value
    .group_segment_fixed_size: 34816
    .kernarg_segment_align: 8
    .kernarg_segment_size: 1136
    .language:       OpenCL C
    .language_version:
      - 2
      - 0
    .max_flat_workgroup_size: 256
    .name:           _Z14gemm_nt_kernelILi2EEv8GemmArgs
    .private_segment_fixed_size: 0
    .sgpr_count:     68
    .sgpr_spill_count: 0
    .symbol:         _Z14gemm_nt_kernelILi2EEv8GemmArgs.kd
    .uniform_work_group_size: 1
    .uses_dynamic_stack: false
    .vgpr_count:     140
    .vgpr_spill_count: 0
    .wavefront_size: 64
  - .agpr_count:     0
    .args:
      - .actual_access:  read_only
        .address_space:  global
        .offset:         0
        .size:           8
        .value_kind:     global_buffer
      - .offset:         8
        .size:           8
        .value_kind:     by_value
      - .actual_access:  read_only
        .address_space:  global
        .offset:         16
        .size:           8
        .value_kind:     global_buffer
      - .actual_access:  read_only
        .address_space:  global
        .offset:         24
        .size:           8
        .value_kind:     global_buffer
      - .actual_access:  read_only
        .address_space:  global
        .offset:         32
        .size:           8
        .value_kind:     global_buffer
      - .actual_access:  read_only
        .address_space:  global
        .offset:         40
        .size:           8
        .value_kind:     global_buffer
      - .actual_access:  write_only
        .address_space:  global
        .offset:         48
        .size:           8
        .value_kind:     global_buffer
      - .actual_access:  write_only
        .address_space:  global
        .offset:         56
        .size:           8
        .value_kind:     global_buffer
      - .offset:         64
        .size:           4
        .value_kind:     by_value
      - .offset:         72
        .size:           376
        .value_kind:     by_value
    .group_segment_fixed_size: 63488
    .kernarg_segment_align: 8
    .kernarg_segment_size: 448
    .language:       OpenCL C
    .language_version:
      - 2
      - 0
    .max_flat_workgroup_size: 512
    .name:           _Z15gru_mfma_kernelILi1EEvPKfmS1_S1_S1_S1_PfS2_i7PreArgs
    .private_segment_fixed_size: 0
    .sgpr_count:     36
    .sgpr_spill_count: 0
    .symbol:         _Z15gru_mfma_kernelILi1EEvPKfmS1_S1_S1_S1_PfS2_i7PreArgs.kd
    .uniform_work_group_size: 1
    .uses_dynamic_stack: false
    .vgpr_count:     232
    .vgpr_spill_count: 0
    .wavefront_size: 64
  - .agpr_count:     0
    .args:
      - .actual_access:  read_only
        .address_space:  global
        .offset:         0
        .size:           8
        .value_kind:     global_buffer
      - .offset:         8
        .size:           8
        .value_kind:     by_value
      - .actual_access:  read_only
        .address_space:  global
        .offset:         16
        .size:           8
        .value_kind:     global_buffer
      - .actual_access:  read_only
        .address_space:  global
        .offset:         24
        .size:           8
        .value_kind:     global_buffer
      - .actual_access:  read_only
        .address_space:  global
        .offset:         32
        .size:           8
        .value_kind:     global_buffer
      - .actual_access:  read_only
        .address_space:  global
        .offset:         40
        .size:           8
        .value_kind:     global_buffer
      - .actual_access:  write_only
        .address_space:  global
        .offset:         48
        .size:           8
        .value_kind:     global_buffer
      - .actual_access:  write_only
        .address_space:  global
        .offset:         56
        .size:           8
        .value_kind:     global_buffer
      - .offset:         64
        .size:           4
        .value_kind:     by_value
      - .offset:         72
        .size:           376
        .value_kind:     by_value
    .group_segment_fixed_size: 64480
    .kernarg_segment_align: 8
    .kernarg_segment_size: 448
    .language:       OpenCL C
    .language_version:
      - 2
      - 0
    .max_flat_workgroup_size: 512
    .name:           _Z15gru_mfma_kernelILi2EEvPKfmS1_S1_S1_S1_PfS2_i7PreArgs
    .private_segment_fixed_size: 0
    .sgpr_count:     50
    .sgpr_spill_count: 0
    .symbol:         _Z15gru_mfma_kernelILi2EEvPKfmS1_S1_S1_S1_PfS2_i7PreArgs.kd
    .uniform_work_group_size: 1
    .uses_dynamic_stack: false
    .vgpr_count:     232
    .vgpr_spill_count: 0
    .wavefront_size: 64
